# s12 + MIX: attention and x3 y-tile stores write-through (sc1)
# baseline (speedup 1.0000x reference)
.LBB0_430:
	s_nop 0
	v_cvt_f32_f16_e32 v2, v142
	v_cvt_f32_f16_sdwa v4, v142 dst_sel:DWORD dst_unused:UNUSED_PAD src0_sel:WORD_1
	v_cvt_f32_f16_e32 v5, v143
	v_mov_b32_e32 v1, v250
	v_mul_f32_e32 v2, 0xbfb8aa3b, v2
	v_exp_f32_e32 v2, v2
	v_mul_f32_e32 v4, 0xbfb8aa3b, v4
	v_exp_f32_e32 v4, v4
	v_add_f32_e32 v2, 1.0, v2
	v_rcp_f32_e32 v30, v2
	v_mul_f32_e32 v2, 0xbfb8aa3b, v5
	v_cvt_f32_f16_sdwa v5, v143 dst_sel:DWORD dst_unused:UNUSED_PAD src0_sel:WORD_1
	v_exp_f32_e32 v2, v2
	v_add_f32_e32 v4, 1.0, v4
	v_rcp_f32_e32 v31, v4
	v_mul_f32_e32 v5, 0xbfb8aa3b, v5
	v_cvt_f32_f16_e32 v4, v144
	v_exp_f32_e32 v5, v5
	v_add_f32_e32 v2, 1.0, v2
	v_rcp_f32_e32 v34, v2
	v_mul_f32_e32 v2, 0xbfb8aa3b, v4
	v_add_f32_e32 v4, 1.0, v5
	v_cvt_f32_f16_sdwa v5, v144 dst_sel:DWORD dst_unused:UNUSED_PAD src0_sel:WORD_1
	v_exp_f32_e32 v2, v2
	v_rcp_f32_e32 v35, v4
	v_cvt_f32_f16_e32 v4, v145
	v_mul_f32_e32 v5, 0xbfb8aa3b, v5
	v_exp_f32_e32 v5, v5
	v_add_f32_e32 v2, 1.0, v2
	v_rcp_f32_e32 v58, v2
	v_mul_f32_e32 v2, 0xbfb8aa3b, v4
	v_add_f32_e32 v4, 1.0, v5
	v_cvt_f32_f16_sdwa v5, v145 dst_sel:DWORD dst_unused:UNUSED_PAD src0_sel:WORD_1
	v_exp_f32_e32 v2, v2
	v_rcp_f32_e32 v59, v4
	v_cvt_f32_f16_e32 v4, v138
	v_mul_f32_e32 v5, 0xbfb8aa3b, v5
	v_exp_f32_e32 v5, v5
	v_add_f32_e32 v2, 1.0, v2
	v_rcp_f32_e32 v48, v2
	v_mul_f32_e32 v2, 0xbfb8aa3b, v4
	v_add_f32_e32 v4, 1.0, v5
	v_cvt_f32_f16_sdwa v5, v138 dst_sel:DWORD dst_unused:UNUSED_PAD src0_sel:WORD_1
	v_exp_f32_e32 v2, v2
	v_rcp_f32_e32 v49, v4
	v_cvt_f32_f16_e32 v4, v139
	v_mul_f32_e32 v5, 0xbfb8aa3b, v5
	v_exp_f32_e32 v5, v5
	v_add_f32_e32 v2, 1.0, v2
	v_rcp_f32_e32 v26, v2
	v_mul_f32_e32 v2, 0xbfb8aa3b, v4
	v_add_f32_e32 v4, 1.0, v5
	v_cvt_f32_f16_sdwa v5, v139 dst_sel:DWORD dst_unused:UNUSED_PAD src0_sel:WORD_1
	v_exp_f32_e32 v2, v2
	v_rcp_f32_e32 v27, v4
	v_cvt_f32_f16_e32 v4, v140
	v_mul_f32_e32 v5, 0xbfb8aa3b, v5
	v_exp_f32_e32 v5, v5
	v_add_f32_e32 v2, 1.0, v2
	v_rcp_f32_e32 v28, v2
	v_mul_f32_e32 v2, 0xbfb8aa3b, v4
	v_add_f32_e32 v4, 1.0, v5
	v_cvt_f32_f16_sdwa v5, v140 dst_sel:DWORD dst_unused:UNUSED_PAD src0_sel:WORD_1
	v_exp_f32_e32 v2, v2
	v_rcp_f32_e32 v29, v4
	v_cvt_f32_f16_e32 v4, v141
	v_mul_f32_e32 v5, 0xbfb8aa3b, v5
	v_exp_f32_e32 v5, v5
	v_add_f32_e32 v2, 1.0, v2
	v_rcp_f32_e32 v32, v2
	v_mul_f32_e32 v2, 0xbfb8aa3b, v4
	v_add_f32_e32 v4, 1.0, v5
	v_cvt_f32_f16_sdwa v5, v141 dst_sel:DWORD dst_unused:UNUSED_PAD src0_sel:WORD_1
	v_exp_f32_e32 v2, v2
	v_rcp_f32_e32 v33, v4
	v_cvt_f32_f16_e32 v4, v134
	v_mul_f32_e32 v5, 0xbfb8aa3b, v5
	v_exp_f32_e32 v5, v5
	v_add_f32_e32 v2, 1.0, v2
	v_rcp_f32_e32 v36, v2
	v_mul_f32_e32 v2, 0xbfb8aa3b, v4
	v_add_f32_e32 v4, 1.0, v5
	v_cvt_f32_f16_sdwa v5, v134 dst_sel:DWORD dst_unused:UNUSED_PAD src0_sel:WORD_1
	v_exp_f32_e32 v2, v2
	v_rcp_f32_e32 v37, v4
	v_cvt_f32_f16_e32 v4, v135
	v_mul_f32_e32 v5, 0xbfb8aa3b, v5
	v_exp_f32_e32 v5, v5
	v_add_f32_e32 v2, 1.0, v2
	v_rcp_f32_e32 v44, v2
	v_mul_f32_e32 v2, 0xbfb8aa3b, v4
	v_exp_f32_e32 v2, v2
	v_add_f32_e32 v4, 1.0, v5
	v_rcp_f32_e32 v45, v4
	v_cvt_f32_f16_sdwa v4, v135 dst_sel:DWORD dst_unused:UNUSED_PAD src0_sel:WORD_1
	v_cvt_f32_f16_e32 v5, v136
	v_add_f32_e32 v2, 1.0, v2
	v_rcp_f32_e32 v60, v2
	v_mul_f32_e32 v2, 0xbfb8aa3b, v4
	v_exp_f32_e32 v2, v2
	v_mul_f32_e32 v4, 0xbfb8aa3b, v5
	v_exp_f32_e32 v4, v4
	v_cvt_f32_f16_sdwa v5, v136 dst_sel:DWORD dst_unused:UNUSED_PAD src0_sel:WORD_1
	v_add_f32_e32 v2, 1.0, v2
	v_rcp_f32_e32 v61, v2
	v_add_f32_e32 v2, 1.0, v4
	v_mul_f32_e32 v4, 0xbfb8aa3b, v5
	v_cvt_f32_f16_e32 v5, v137
	v_exp_f32_e32 v4, v4
	v_rcp_f32_e32 v136, v2
	v_cvt_f32_f16_sdwa v2, v137 dst_sel:DWORD dst_unused:UNUSED_PAD src0_sel:WORD_1
	v_mul_f32_e32 v5, 0xbfb8aa3b, v5
	v_exp_f32_e32 v5, v5
	v_add_f32_e32 v4, 1.0, v4
	v_mul_f32_e32 v2, 0xbfb8aa3b, v2
	v_exp_f32_e32 v2, v2
	v_rcp_f32_e32 v137, v4
	v_add_f32_e32 v4, 1.0, v5
	v_rcp_f32_e32 v146, v4
	v_cvt_f32_f16_e32 v4, v130
	v_add_f32_e32 v2, 1.0, v2
	v_ashrrev_i32_e32 v0, 2, v1
	v_lshlrev_b32_e32 v1, 5, v1
	v_add_u32_e32 v0, 16, v0
	v_and_b32_e32 v12, 0x60, v1
	v_mul_lo_u32 v3, v0, s44
	v_lshlrev_b32_e32 v96, 1, v12
	v_rcp_f32_e32 v147, v2
	v_mul_f32_e32 v2, 0xbfb8aa3b, v4
	v_add3_u32 v3, s5, v3, v96
	v_exp_f32_e32 v2, v2
	ds_read_b128 v[142:145], v3 offset:16384
	ds_read_b128 v[22:25], v3 offset:16400
	v_cvt_f32_f16_sdwa v4, v130 dst_sel:DWORD dst_unused:UNUSED_PAD src0_sel:WORD_1
	ds_read_b128 v[18:21], v3 offset:16416
	ds_read_b128 v[8:11], v3 offset:16432
	v_cvt_f32_f16_e32 v3, v131
	v_add_f32_e32 v2, 1.0, v2
	v_mul_f32_e32 v4, 0xbfb8aa3b, v4
	v_rcp_f32_e32 v46, v2
	v_mul_f32_e32 v2, 0xbfb8aa3b, v3
	v_exp_f32_e32 v4, v4
	v_exp_f32_e32 v2, v2
	v_cvt_f32_f16_e32 v5, v133
	v_cvt_f32_f16_sdwa v6, v133 dst_sel:DWORD dst_unused:UNUSED_PAD src0_sel:WORD_1
	v_add_f32_e32 v3, 1.0, v4
	v_add_f32_e32 v2, 1.0, v2
	v_rcp_f32_e32 v47, v3
	v_cvt_f32_f16_sdwa v3, v131 dst_sel:DWORD dst_unused:UNUSED_PAD src0_sel:WORD_1
	v_rcp_f32_e32 v50, v2
	v_cvt_f32_f16_e32 v2, v132
	v_cvt_f32_f16_sdwa v4, v132 dst_sel:DWORD dst_unused:UNUSED_PAD src0_sel:WORD_1
	v_mul_f32_e32 v3, 0xbfb8aa3b, v3
	v_exp_f32_e32 v3, v3
	v_mul_f32_e32 v2, 0xbfb8aa3b, v2
	v_mul_f32_e32 v4, 0xbfb8aa3b, v4
	v_exp_f32_e32 v2, v2
	v_exp_f32_e32 v4, v4
	v_mul_f32_e32 v5, 0xbfb8aa3b, v5
	v_add_f32_e32 v13, 1.0, v3
	v_add_f32_e32 v2, 1.0, v2
	v_add_f32_e32 v3, 1.0, v4
	v_exp_f32_e32 v7, v5
	v_mul_f32_e32 v5, 0xbfb8aa3b, v6
	v_rcp_f32_e32 v2, v2
	v_rcp_f32_e32 v3, v3
	s_waitcnt lgkmcnt(0)
	v_cvt_f32_f16_e32 v4, v10
	v_exp_f32_e32 v14, v5
	v_cvt_f32_f16_sdwa v5, v10 dst_sel:DWORD dst_unused:UNUSED_PAD src0_sel:WORD_1
	v_cvt_f32_f16_e32 v132, v143
	v_cvt_f32_f16_sdwa v133, v143 dst_sel:DWORD dst_unused:UNUSED_PAD src0_sel:WORD_1
	v_cvt_f32_f16_sdwa v131, v127 dst_sel:DWORD dst_unused:UNUSED_PAD src0_sel:WORD_1
	v_cvt_f32_f16_e32 v130, v127
	v_ashrrev_i32_e32 v1, 31, v0
	v_pk_mul_f32 v[42:43], v[2:3], v[4:5]
	v_lshl_add_u64 v[0:1], s[42:43], 0, v[0:1]
	v_mov_b64_e32 v[2:3], s[20:21]
	v_pk_mul_f32 v[132:133], v[34:35], v[132:133]
	v_mul_f32_e32 v35, 0xbfb8aa3b, v131
	v_mad_u64_u32 v[2:3], s[10:11], v0, s7, v[2:3]
	v_mul_f32_e32 v34, 0xbfb8aa3b, v130
	v_exp_f32_e32 v35, v35
	v_mov_b32_e32 v0, v3
	v_exp_f32_e32 v34, v34
	v_cvt_f32_f16_e32 v140, v126
	v_mad_u64_u32 v[0:1], s[10:11], v1, s7, v[0:1]
	v_mov_b32_e32 v3, v0
	v_lshl_add_u64 v[40:41], v[2:3], 0, v[96:97]
	v_add_f32_e32 v96, 1.0, v35
	v_add_f32_e32 v34, 1.0, v34
	v_rcp_f32_e32 v135, v96
	v_mul_f32_e32 v96, 0xbfb8aa3b, v140
	v_rcp_f32_e32 v134, v34
	v_cvt_f32_f16_e32 v34, v142
	v_cvt_f32_f16_sdwa v35, v142 dst_sel:DWORD dst_unused:UNUSED_PAD src0_sel:WORD_1
	v_exp_f32_e32 v96, v96
	v_cvt_f32_f16_sdwa v141, v126 dst_sel:DWORD dst_unused:UNUSED_PAD src0_sel:WORD_1
	v_cvt_f32_f16_e32 v126, v129
	v_pk_mul_f32 v[142:143], v[30:31], v[34:35]
	v_add_f32_e32 v30, 1.0, v96
	v_rcp_f32_e32 v148, v30
	v_mul_f32_e32 v30, 0xbfb8aa3b, v141
	v_exp_f32_e32 v30, v30
	v_mul_f32_e32 v31, 0xbfb8aa3b, v126
	v_cvt_f32_f16_sdwa v127, v129 dst_sel:DWORD dst_unused:UNUSED_PAD src0_sel:WORD_1
	v_exp_f32_e32 v31, v31
	v_add_f32_e32 v30, 1.0, v30
	v_rcp_f32_e32 v149, v30
	v_mul_f32_e32 v30, 0xbfb8aa3b, v127
	v_cvt_f32_f16_e32 v56, v145
	v_cvt_f32_f16_sdwa v57, v145 dst_sel:DWORD dst_unused:UNUSED_PAD src0_sel:WORD_1
	v_add_f32_e32 v34, 1.0, v31
	v_exp_f32_e32 v35, v30
	v_cvt_f32_f16_e32 v30, v25
	v_cvt_f32_f16_sdwa v31, v25 dst_sel:DWORD dst_unused:UNUSED_PAD src0_sel:WORD_1
	v_cvt_f32_f16_e32 v150, v124
	v_cvt_f32_f16_sdwa v151, v124 dst_sel:DWORD dst_unused:UNUSED_PAD src0_sel:WORD_1
	v_pk_mul_f32 v[48:49], v[48:49], v[56:57]
	v_cvt_f32_f16_e32 v56, v128
	v_cvt_f32_f16_sdwa v57, v128 dst_sel:DWORD dst_unused:UNUSED_PAD src0_sel:WORD_1
	v_add_f32_e32 v25, 1.0, v35
	v_pk_mul_f32 v[128:129], v[36:37], v[30:31]
	v_cvt_f32_f16_e32 v30, v24
	v_cvt_f32_f16_sdwa v31, v24 dst_sel:DWORD dst_unused:UNUSED_PAD src0_sel:WORD_1
	v_mul_f32_e32 v24, 0xbfb8aa3b, v150
	v_rcp_f32_e32 v153, v25
	v_exp_f32_e32 v24, v24
	v_mul_f32_e32 v25, 0xbfb8aa3b, v151
	v_exp_f32_e32 v25, v25
	v_add_f32_e32 v6, 1.0, v7
	v_add_f32_e32 v7, 1.0, v14
	v_add_f32_e32 v24, 1.0, v24
	v_cvt_f32_f16_e32 v160, v123
	v_rcp_f32_e32 v6, v6
	v_rcp_f32_e32 v7, v7
	v_cvt_f32_f16_e32 v10, v11
	v_cvt_f32_f16_sdwa v11, v11 dst_sel:DWORD dst_unused:UNUSED_PAD src0_sel:WORD_1
	v_pk_mul_f32 v[154:155], v[32:33], v[30:31]
	v_rcp_f32_e32 v158, v24
	v_add_f32_e32 v30, 1.0, v25
	v_cvt_f32_f16_e32 v24, v23
	v_cvt_f32_f16_sdwa v25, v23 dst_sel:DWORD dst_unused:UNUSED_PAD src0_sel:WORD_1
	v_cvt_f32_f16_sdwa v161, v123 dst_sel:DWORD dst_unused:UNUSED_PAD src0_sel:WORD_1
	v_lshlrev_b32_e32 v184, 2, v12
	v_mul_f32_e32 v23, 0xbfb8aa3b, v160
	v_rcp_f32_e32 v51, v13
	v_pk_mul_f32 v[38:39], v[6:7], v[10:11]
	global_load_dwordx4 v[0:3], v184, s[14:15] offset:48
	global_load_dwordx4 v[4:7], v184, s[14:15] offset:32
	global_load_dwordx4 v[10:13], v184, s[14:15] offset:16
	global_load_dwordx4 v[14:17], v184, s[14:15]
	v_pk_mul_f32 v[164:165], v[28:29], v[24:25]
	v_exp_f32_e32 v23, v23
	v_mul_f32_e32 v24, 0xbfb8aa3b, v161
	v_exp_f32_e32 v24, v24
	v_cvt_f32_f16_e32 v168, v122
	v_cvt_f32_f16_sdwa v169, v122 dst_sel:DWORD dst_unused:UNUSED_PAD src0_sel:WORD_1
	v_add_f32_e32 v23, 1.0, v23
	v_rcp_f32_e32 v166, v23
	v_add_f32_e32 v23, 1.0, v24
	v_cvt_f32_f16_e32 v24, v22
	v_cvt_f32_f16_sdwa v25, v22 dst_sel:DWORD dst_unused:UNUSED_PAD src0_sel:WORD_1
	v_mul_f32_e32 v22, 0xbfb8aa3b, v168
	v_rcp_f32_e32 v167, v23
	v_exp_f32_e32 v22, v22
	v_mul_f32_e32 v23, 0xbfb8aa3b, v169
	v_exp_f32_e32 v23, v23
	v_cvt_f32_f16_e32 v124, v125
	v_cvt_f32_f16_sdwa v125, v125 dst_sel:DWORD dst_unused:UNUSED_PAD src0_sel:WORD_1
	v_add_f32_e32 v22, 1.0, v22
	v_rcp_f32_e32 v172, v22
	v_add_f32_e32 v22, 1.0, v23
	v_mul_f32_e32 v23, 0xbfb8aa3b, v124
	v_pk_mul_f32 v[122:123], v[26:27], v[24:25]
	v_exp_f32_e32 v23, v23
	v_mul_f32_e32 v24, 0xbfb8aa3b, v125
	v_exp_f32_e32 v24, v24
	v_rcp_f32_e32 v173, v22
	v_add_f32_e32 v22, 1.0, v23
	v_rcp_f32_e32 v174, v22
	v_add_f32_e32 v22, 1.0, v24
	v_rcp_f32_e32 v152, v34
	v_rcp_f32_e32 v159, v30
	v_rcp_f32_e32 v175, v22
	global_load_dwordx4 v[22:25], v184, s[14:15] offset:112
	global_load_dwordx4 v[26:29], v184, s[14:15] offset:96
	global_load_dwordx4 v[30:33], v184, s[14:15] offset:80
	global_load_dwordx4 v[34:37], v184, s[14:15] offset:64
	v_cvt_f32_f16_e32 v182, v21
	v_cvt_f32_f16_sdwa v183, v21 dst_sel:DWORD dst_unused:UNUSED_PAD src0_sel:WORD_1
	v_cvt_f32_f16_e32 v62, v144
	v_cvt_f32_f16_sdwa v63, v144 dst_sel:DWORD dst_unused:UNUSED_PAD src0_sel:WORD_1
	v_cvt_f32_f16_sdwa v21, v120 dst_sel:DWORD dst_unused:UNUSED_PAD src0_sel:WORD_1
	v_pk_mul_f32 v[146:147], v[146:147], v[182:183]
	v_cvt_f32_f16_e32 v182, v20
	v_cvt_f32_f16_sdwa v183, v20 dst_sel:DWORD dst_unused:UNUSED_PAD src0_sel:WORD_1
	v_cvt_f32_f16_e32 v20, v120
	v_pk_mul_f32 v[162:163], v[142:143], v[142:143]
	v_pk_mul_f32 v[156:157], v[132:133], v[132:133]
	v_add_f32_e32 v162, v162, v163
	v_mul_f32_e32 v96, 0xbfb8aa3b, v20
	v_pk_mul_f32 v[58:59], v[58:59], v[62:63]
	v_exp_f32_e32 v96, v96
	v_mul_f32_e32 v120, 0xbfb8aa3b, v21
	v_add_f32_e32 v156, v156, v162
	v_pk_mul_f32 v[144:145], v[58:59], v[58:59]
	v_exp_f32_e32 v120, v120
	v_cvt_f32_f16_e32 v190, v119
	v_add_f32_e32 v156, v157, v156
	v_cvt_f32_f16_sdwa v191, v119 dst_sel:DWORD dst_unused:UNUSED_PAD src0_sel:WORD_1
	v_add_f32_e32 v144, v144, v156
	v_pk_mul_f32 v[138:139], v[48:49], v[48:49]
	v_add_f32_e32 v144, v145, v144
	v_add_f32_e32 v96, 1.0, v96
	v_add_f32_e32 v138, v138, v144
	v_pk_mul_f32 v[180:181], v[122:123], v[122:123]
	v_rcp_f32_e32 v186, v96
	v_add_f32_e32 v96, 1.0, v120
	v_cvt_f32_f16_e32 v188, v19
	v_cvt_f32_f16_sdwa v189, v19 dst_sel:DWORD dst_unused:UNUSED_PAD src0_sel:WORD_1
	v_mul_f32_e32 v19, 0xbfb8aa3b, v190
	v_add_f32_e32 v138, v139, v138
	v_rcp_f32_e32 v187, v96
	v_exp_f32_e32 v19, v19
	v_mul_f32_e32 v96, 0xbfb8aa3b, v191
	v_add_f32_e32 v138, v180, v138
	v_pk_mul_f32 v[178:179], v[164:165], v[164:165]
	v_exp_f32_e32 v96, v96
	v_cvt_f32_f16_e32 v194, v118
	v_add_f32_e32 v138, v181, v138
	v_cvt_f32_f16_e32 v196, v18
	v_cvt_f32_f16_sdwa v197, v18 dst_sel:DWORD dst_unused:UNUSED_PAD src0_sel:WORD_1
	v_add_f32_e32 v138, v178, v138
	v_pk_mul_f32 v[176:177], v[154:155], v[154:155]
	v_add_f32_e32 v138, v179, v138
	v_add_f32_e32 v19, 1.0, v19
	v_add_f32_e32 v138, v176, v138
	v_pk_mul_f32 v[170:171], v[128:129], v[128:129]
	v_rcp_f32_e32 v192, v19
	v_add_f32_e32 v19, 1.0, v96
	v_mul_f32_e32 v18, 0xbfb8aa3b, v194
	v_add_f32_e32 v138, v177, v138
	v_rcp_f32_e32 v193, v19
	v_exp_f32_e32 v96, v18
	v_pk_mul_f32 v[18:19], v[44:45], v[196:197]
	v_add_f32_e32 v138, v170, v138
	v_pk_mul_f32 v[44:45], v[18:19], v[18:19]
	v_add_f32_e32 v138, v171, v138
	v_pk_mul_f32 v[60:61], v[60:61], v[188:189]
	v_add_f32_e32 v44, v44, v138
	v_pk_mul_f32 v[188:189], v[60:61], v[60:61]
	v_add_f32_e32 v44, v45, v44
	v_pk_mul_f32 v[136:137], v[136:137], v[182:183]
	v_cvt_f32_f16_e32 v200, v8
	v_cvt_f32_f16_sdwa v201, v8 dst_sel:DWORD dst_unused:UNUSED_PAD src0_sel:WORD_1
	v_add_f32_e32 v44, v188, v44
	v_pk_mul_f32 v[182:183], v[136:137], v[136:137]
	v_cvt_f32_f16_e32 v198, v9
	v_cvt_f32_f16_sdwa v199, v9 dst_sel:DWORD dst_unused:UNUSED_PAD src0_sel:WORD_1
	v_add_f32_e32 v44, v189, v44
	v_add_f32_e32 v44, v182, v44
	v_pk_mul_f32 v[184:185], v[146:147], v[146:147]
	v_add_f32_e32 v44, v183, v44
	v_pk_mul_f32 v[46:47], v[46:47], v[200:201]
	v_add_f32_e32 v44, v184, v44
	v_pk_mul_f32 v[50:51], v[50:51], v[198:199]
	v_pk_mul_f32 v[198:199], v[46:47], v[46:47]
	v_add_f32_e32 v44, v185, v44
	v_add_f32_e32 v44, v198, v44
	v_pk_mul_f32 v[8:9], v[50:51], v[50:51]
	v_add_f32_e32 v44, v199, v44
	v_cvt_f32_f16_sdwa v195, v118 dst_sel:DWORD dst_unused:UNUSED_PAD src0_sel:WORD_1
	v_add_f32_e32 v8, v8, v44
	v_pk_mul_f32 v[52:53], v[42:43], v[42:43]
	v_add_f32_e32 v8, v9, v8
	v_add_f32_e32 v8, v52, v8
	v_pk_mul_f32 v[54:55], v[38:39], v[38:39]
	v_cvt_f32_f16_e32 v118, v121
	v_add_f32_e32 v8, v53, v8
	v_mul_f32_e32 v119, 0xbfb8aa3b, v195
	v_add_f32_e32 v8, v54, v8
	v_exp_f32_e32 v119, v119
	v_add_f32_e32 v8, v55, v8
	v_add_f32_e32 v96, 1.0, v96
	ds_swizzle_b32 v9, v8 offset:swizzle(SWAP,1)
	v_rcp_f32_e32 v120, v96
	v_mul_f32_e32 v96, 0xbfb8aa3b, v118
	v_exp_f32_e32 v96, v96
	v_add_f32_e32 v196, 1.0, v119
	v_cvt_f32_f16_sdwa v119, v121 dst_sel:DWORD dst_unused:UNUSED_PAD src0_sel:WORD_1
	v_cvt_f32_f16_e32 v200, v114
	s_waitcnt lgkmcnt(0)
	v_add_f32_e32 v8, v8, v9
	v_add_f32_e32 v96, 1.0, v96
	ds_swizzle_b32 v9, v8 offset:swizzle(SWAP,2)
	v_rcp_f32_e32 v121, v196
	v_rcp_f32_e32 v196, v96
	v_mul_f32_e32 v96, 0xbfb8aa3b, v119
	v_exp_f32_e32 v96, v96
	v_mul_f32_e32 v45, 0xbfb8aa3b, v200
	v_cvt_f32_f16_sdwa v201, v114 dst_sel:DWORD dst_unused:UNUSED_PAD src0_sel:WORD_1
	v_exp_f32_e32 v45, v45
	s_waitcnt lgkmcnt(0)
	v_add_f32_e32 v8, v8, v9
	v_add_f32_e32 v44, 1.0, v96
	v_fmamk_f32 v8, v8, 0x3c000000, v242
	v_rcp_f32_e32 v197, v44
	v_add_f32_e32 v44, 1.0, v45
	v_mul_f32_e32 v45, 0xbfb8aa3b, v201
	v_mul_f32_e32 v9, 0x4b800000, v8
	v_cmp_gt_f32_e32 vcc, s34, v8
	v_exp_f32_e32 v45, v45
	v_mul_f32_e32 v62, 0xbfb8aa3b, v56
	v_cndmask_b32_e32 v8, v8, v9, vcc
	v_rsq_f32_e32 v8, v8
	v_mul_f32_e32 v63, 0xbfb8aa3b, v57
	v_exp_f32_e32 v62, v62
	v_exp_f32_e32 v63, v63
	v_add_f32_e32 v9, 1.0, v45
	v_rcp_f32_e32 v45, v9
	v_mul_f32_e32 v9, 0x45800000, v8
	v_cndmask_b32_e32 v52, v8, v9, vcc
	v_pk_mul_f32 v[8:9], v[142:143], v[52:53] op_sel_hi:[1,0]
	v_add_f32_e32 v62, 1.0, v62
	v_add_f32_e32 v63, 1.0, v63
	s_waitcnt vmcnt(4)
	v_pk_mul_f32 v[8:9], v[14:15], v[8:9]
	v_pk_mul_f32 v[14:15], v[132:133], v[52:53] op_sel_hi:[1,0]
	v_rcp_f32_e32 v62, v62
	v_rcp_f32_e32 v63, v63
	v_pk_mul_f32 v[14:15], v[16:17], v[14:15]
	v_pk_mul_f32 v[16:17], v[58:59], v[52:53] op_sel_hi:[1,0]
	v_pk_mul_f32 v[8:9], v[8:9], v[140:141]
	v_pk_mul_f32 v[10:11], v[10:11], v[16:17]
	v_pk_mul_f32 v[16:17], v[48:49], v[52:53] op_sel_hi:[1,0]
	v_pk_mul_f32 v[14:15], v[14:15], v[130:131]
	v_pk_mul_f32 v[12:13], v[12:13], v[16:17]
	v_pk_mul_f32 v[10:11], v[10:11], v[56:57]
	v_pk_mul_f32 v[12:13], v[12:13], v[126:127]
	v_pk_mul_f32 v[8:9], v[148:149], v[8:9]
	v_pk_mul_f32 v[14:15], v[134:135], v[14:15]
	v_pk_mul_f32 v[10:11], v[62:63], v[10:11]
	v_pk_mul_f32 v[12:13], v[152:153], v[12:13]
	v_cvt_pk_f16_f32 v8, v8, v9
	v_cvt_pk_f16_f32 v9, v14, v15
	v_cvt_pk_f16_f32 v10, v10, v11
	v_cvt_pk_f16_f32 v11, v12, v13
	global_store_dwordx4 v[40:41], v[8:11], off offset:2048 sc1
	v_rcp_f32_e32 v44, v44
	s_mov_b32 s6, 32
	v_pk_mul_f32 v[8:9], v[122:123], v[52:53] op_sel_hi:[1,0]
	s_and_b64 vcc, exec, s[38:39]
	v_pk_mul_f32 v[4:5], v[4:5], v[8:9]
	v_pk_mul_f32 v[8:9], v[164:165], v[52:53] op_sel_hi:[1,0]
	v_pk_mul_f32 v[4:5], v[4:5], v[168:169]
	v_pk_mul_f32 v[6:7], v[6:7], v[8:9]
	v_pk_mul_f32 v[8:9], v[154:155], v[52:53] op_sel_hi:[1,0]
	v_pk_mul_f32 v[6:7], v[6:7], v[160:161]
	v_pk_mul_f32 v[0:1], v[0:1], v[8:9]
	v_pk_mul_f32 v[4:5], v[172:173], v[4:5]
	v_pk_mul_f32 v[0:1], v[0:1], v[150:151]
	v_pk_mul_f32 v[6:7], v[166:167], v[6:7]
	v_pk_mul_f32 v[8:9], v[158:159], v[0:1]
	v_pk_mul_f32 v[0:1], v[128:129], v[52:53] op_sel_hi:[1,0]
	s_mov_b64 s[46:47], 0
	v_pk_mul_f32 v[0:1], v[2:3], v[0:1]
	v_cvt_pk_f16_f32 v2, v8, v9
	v_pk_mul_f32 v[0:1], v[0:1], v[124:125]
	v_cvt_f32_f16_e32 v8, v116
	v_pk_mul_f32 v[10:11], v[174:175], v[0:1]
	v_cvt_pk_f16_f32 v0, v4, v5
	v_cvt_pk_f16_f32 v1, v6, v7
	v_cvt_pk_f16_f32 v3, v10, v11
	global_store_dwordx4 v[40:41], v[0:3], off offset:2064 sc1
	v_pk_mul_f32 v[4:5], v[136:137], v[52:53] op_sel_hi:[1,0]
	v_pk_mul_f32 v[6:7], v[146:147], v[52:53] op_sel_hi:[1,0]
	v_pk_mul_f32 v[0:1], v[18:19], v[52:53] op_sel_hi:[1,0]
	v_pk_mul_f32 v[2:3], v[60:61], v[52:53] op_sel_hi:[1,0]
	s_waitcnt vmcnt(2)
	v_pk_mul_f32 v[0:1], v[34:35], v[0:1]
	v_pk_mul_f32 v[2:3], v[36:37], v[2:3]
	v_pk_mul_f32 v[4:5], v[30:31], v[4:5]
	v_pk_mul_f32 v[0:1], v[0:1], v[194:195]
	v_pk_mul_f32 v[2:3], v[2:3], v[190:191]
	v_pk_mul_f32 v[4:5], v[4:5], v[20:21]
	v_pk_mul_f32 v[0:1], v[120:121], v[0:1]
	v_pk_mul_f32 v[2:3], v[192:193], v[2:3]
	v_pk_mul_f32 v[4:5], v[186:187], v[4:5]
	v_pk_mul_f32 v[6:7], v[32:33], v[6:7]
	v_cvt_pk_f16_f32 v0, v0, v1
	v_cvt_pk_f16_f32 v1, v2, v3
	v_cvt_pk_f16_f32 v2, v4, v5
	v_cvt_f32_f16_e32 v4, v115
	v_cvt_f32_f16_sdwa v5, v115 dst_sel:DWORD dst_unused:UNUSED_PAD src0_sel:WORD_1
	v_pk_mul_f32 v[6:7], v[6:7], v[118:119]
	v_mul_f32_e32 v9, 0xbfb8aa3b, v8
	v_pk_mul_f32 v[6:7], v[196:197], v[6:7]
	v_exp_f32_e32 v10, v9
	v_cvt_pk_f16_f32 v3, v6, v7
	global_store_dwordx4 v[40:41], v[0:3], off offset:2080 sc1
	v_cvt_f32_f16_sdwa v9, v116 dst_sel:DWORD dst_unused:UNUSED_PAD src0_sel:WORD_1
	v_pk_mul_f32 v[6:7], v[50:51], v[52:53] op_sel_hi:[1,0]
	v_mul_f32_e32 v2, 0xbfb8aa3b, v4
	v_mul_f32_e32 v3, 0xbfb8aa3b, v5
	v_exp_f32_e32 v2, v2
	v_exp_f32_e32 v3, v3
	v_pk_mul_f32 v[6:7], v[28:29], v[6:7]
	v_pk_mul_f32 v[0:1], v[46:47], v[52:53] op_sel_hi:[1,0]
	v_add_f32_e32 v2, 1.0, v2
	v_add_f32_e32 v3, 1.0, v3
	v_rcp_f32_e32 v2, v2
	v_rcp_f32_e32 v3, v3
	v_pk_mul_f32 v[4:5], v[6:7], v[4:5]
	v_pk_mul_f32 v[6:7], v[42:43], v[52:53] op_sel_hi:[1,0]
	v_pk_mul_f32 v[0:1], v[26:27], v[0:1]
	v_pk_mul_f32 v[2:3], v[2:3], v[4:5]
	v_mul_f32_e32 v5, 0xbfb8aa3b, v9
	v_pk_mul_f32 v[6:7], v[22:23], v[6:7]
	v_exp_f32_e32 v5, v5
	v_pk_mul_f32 v[6:7], v[6:7], v[8:9]
	v_cvt_f32_f16_e32 v8, v117
	v_cvt_f32_f16_sdwa v9, v117 dst_sel:DWORD dst_unused:UNUSED_PAD src0_sel:WORD_1
	v_add_f32_e32 v4, 1.0, v10
	v_add_f32_e32 v5, 1.0, v5
	v_mul_f32_e32 v10, 0xbfb8aa3b, v8
	v_mul_f32_e32 v11, 0xbfb8aa3b, v9
	v_rcp_f32_e32 v4, v4
	v_rcp_f32_e32 v5, v5
	v_exp_f32_e32 v10, v10
	v_exp_f32_e32 v11, v11
	v_pk_mul_f32 v[0:1], v[0:1], v[200:201]
	v_pk_mul_f32 v[4:5], v[4:5], v[6:7]
	v_add_f32_e32 v6, 1.0, v10
	v_add_f32_e32 v7, 1.0, v11
	v_rcp_f32_e32 v6, v6
	v_rcp_f32_e32 v7, v7
	v_pk_mul_f32 v[10:11], v[38:39], v[52:53] op_sel_hi:[1,0]
	v_pk_mul_f32 v[0:1], v[44:45], v[0:1]
	v_pk_mul_f32 v[10:11], v[24:25], v[10:11]
	v_cvt_pk_f16_f32 v0, v0, v1
	v_pk_mul_f32 v[8:9], v[10:11], v[8:9]
	v_cvt_pk_f16_f32 v1, v2, v3
	v_pk_mul_f32 v[6:7], v[6:7], v[8:9]
	v_cvt_pk_f16_f32 v2, v4, v5
	v_cvt_pk_f16_f32 v3, v6, v7
	global_store_dwordx4 v[40:41], v[0:3], off offset:2096 sc1
	s_waitcnt lgkmcnt(0)
	s_cbranch_vccz .LBB0_428

; __device__ __forceinline__ void x3_wave(int item, int b0, const h16* __restrict__ proj, const float* __restrict__ small, const h16* __restrict__ qkc, const h16* __restrict__ CS, ...
;     ...
;         for (int g = 0; g < 4; ++g) { const f32x4 dn = *(lds_cf32x4*)(R + W_SC + 1024 + (32 * tb + 8 * g + 4 * hi) * 4), em = *(lds_cf32x4*)(R + W_SC + 768 + (32 * tb + 8 * g + 4 * hi) * 4);
; #pragma unroll
;             for (int i = 0; i < 4; ++i) { const float inv = __builtin_amdgcn_rcpf(fmaxf(fabsf(dn[i]), em[i])); const int rl = 8 * g + 4 * hi + i;
; #pragma unroll
;                 for (int vb = 0; vb < 4; ++vb) *(__attribute__((address_space(3))) h16*)(R + W_K + rl * 272 + (32 * vb + r32) * 2) = (h16)(acc[vb][4 * g + i] * inv); } }
.LBB0_443:
	v_add_u32_e32 v96, s6, v96
	s_waitcnt lgkmcnt(0)
	v_lshl_add_u32 v188, v96, 2, s5
	ds_read_b128 v[178:181], v188 offset:25856
	ds_read_b128 v[182:185], v188 offset:26112
	s_movk_i32 s6, 0x440
	v_cvt_f32_f16_e32 v192, v155
	v_cvt_f32_f16_sdwa v193, v155 dst_sel:DWORD dst_unused:UNUSED_PAD src0_sel:WORD_1
	s_waitcnt lgkmcnt(1)
	v_max_f32_e32 v96, v178, v178
	s_waitcnt lgkmcnt(0)
	v_max_f32_e64 v178, |v182|, |v182|
	v_max_f32_e32 v96, v178, v96
	v_rcp_f32_e32 v178, v96
	v_lshl_add_u32 v96, v232, 1, s5
	v_mad_u64_u32 v[186:187], s[10:11], v231, s6, v[96:97]
	v_fma_mixlo_f16 v0, v0, v178, 0
	v_fma_mixlo_f16 v16, v16, v178, 0
	ds_write_b16 v186, v0 offset:16384
	ds_write_b16 v186, v16 offset:16448
	v_fma_mixlo_f16 v0, v32, v178, 0
	v_max_f32_e32 v16, v179, v179
	v_max_f32_e64 v32, |v183|, |v183|
	v_max_f32_e32 v16, v32, v16
	v_rcp_f32_e32 v16, v16
	ds_write_b16 v186, v0 offset:16512
	v_fma_mixlo_f16 v0, v48, v178, 0
	ds_write_b16 v186, v0 offset:16576
	v_fma_mixlo_f16 v0, v1, v16, 0
	ds_write_b16 v186, v0 offset:16656
	v_fma_mixlo_f16 v0, v17, v16, 0
	v_max_f32_e32 v1, v180, v180
	v_max_f32_e64 v17, |v184|, |v184|
	v_max_f32_e32 v1, v17, v1
	v_rcp_f32_e32 v1, v1
	ds_write_b16 v186, v0 offset:16720
	v_fma_mixlo_f16 v0, v33, v16, 0
	ds_write_b16 v186, v0 offset:16784
	v_fma_mixlo_f16 v0, v49, v16, 0
	ds_write_b16 v186, v0 offset:16848
	v_fma_mixlo_f16 v0, v2, v1, 0
	v_max_f32_e32 v2, v181, v181
	v_max_f32_e64 v16, |v185|, |v185|
	v_max_f32_e32 v2, v16, v2
	v_rcp_f32_e32 v2, v2
	ds_write_b16 v186, v0 offset:16928
	v_fma_mixlo_f16 v0, v18, v1, 0
	ds_write_b16 v186, v0 offset:16992
	v_fma_mixlo_f16 v0, v34, v1, 0
	ds_write_b16 v186, v0 offset:17056
	v_fma_mixlo_f16 v0, v50, v1, 0
	ds_write_b16 v186, v0 offset:17120
	v_fma_mixlo_f16 v0, v3, v2, 0
	ds_write_b16 v186, v0 offset:17200
	v_fma_mixlo_f16 v0, v19, v2, 0
	ds_write_b16 v186, v0 offset:17264
	v_fma_mixlo_f16 v0, v35, v2, 0
	ds_write_b16 v186, v0 offset:17328
	v_fma_mixlo_f16 v0, v51, v2, 0
	ds_write_b16 v186, v0 offset:17392
	ds_read_b128 v[0:3], v188 offset:25888
	ds_read_b128 v[16:19], v188 offset:26144
	v_mad_u64_u32 v[32:33], s[10:11], v233, s44, v[96:97]
	v_cvt_f32_f16_e32 v182, v156
	s_waitcnt lgkmcnt(1)
	v_max_f32_e32 v0, v0, v0
	s_waitcnt lgkmcnt(0)
	v_max_f32_e64 v16, |v16|, |v16|
	v_max_f32_e32 v0, v16, v0
	v_rcp_f32_e32 v0, v0
	v_max_f32_e32 v1, v1, v1
	v_max_f32_e64 v16, |v17|, |v17|
	v_max_f32_e32 v1, v16, v1
	v_fma_mixlo_f16 v4, v4, v0, 0
	v_rcp_f32_e32 v1, v1
	ds_write_b16 v32, v4 offset:16384
	v_fma_mixlo_f16 v4, v20, v0, 0
	ds_write_b16 v32, v4 offset:16448
	v_fma_mixlo_f16 v4, v36, v0, 0
	ds_write_b16 v32, v4 offset:16512
	v_fma_mixlo_f16 v0, v52, v0, 0
	v_max_f32_e32 v2, v2, v2
	v_max_f32_e64 v4, |v18|, |v18|
	ds_write_b16 v32, v0 offset:16576
	v_fma_mixlo_f16 v0, v5, v1, 0
	v_max_f32_e32 v2, v4, v2
	ds_write_b16 v186, v0 offset:18832
	v_fma_mixlo_f16 v0, v21, v1, 0
	v_rcp_f32_e32 v2, v2
	ds_write_b16 v186, v0 offset:18896
	v_fma_mixlo_f16 v0, v37, v1, 0
	ds_write_b16 v186, v0 offset:18960
	v_fma_mixlo_f16 v0, v53, v1, 0
	v_max_f32_e32 v1, v3, v3
	v_max_f32_e64 v3, |v19|, |v19|
	v_max_f32_e32 v1, v3, v1
	ds_write_b16 v186, v0 offset:19024
	v_fma_mixlo_f16 v0, v6, v2, 0
	v_rcp_f32_e32 v1, v1
	ds_write_b16 v186, v0 offset:19104
	v_fma_mixlo_f16 v0, v22, v2, 0
	ds_write_b16 v186, v0 offset:19168
	v_fma_mixlo_f16 v0, v38, v2, 0
	ds_write_b16 v186, v0 offset:19232
	v_fma_mixlo_f16 v0, v54, v2, 0
	ds_write_b16 v186, v0 offset:19296
	v_fma_mixlo_f16 v0, v7, v1, 0
	ds_write_b16 v186, v0 offset:19376
	v_fma_mixlo_f16 v0, v23, v1, 0
	ds_write_b16 v186, v0 offset:19440
	v_fma_mixlo_f16 v0, v39, v1, 0
	ds_write_b16 v186, v0 offset:19504
	v_fma_mixlo_f16 v0, v55, v1, 0
	ds_write_b16 v186, v0 offset:19568
	ds_read_b128 v[0:3], v188 offset:25920
	ds_read_b128 v[4:7], v188 offset:26176
	v_cvt_f32_f16_sdwa v183, v156 dst_sel:DWORD dst_unused:UNUSED_PAD src0_sel:WORD_1
	v_cvt_f32_f16_e32 v200, v154
	v_cvt_f32_f16_sdwa v201, v154 dst_sel:DWORD dst_unused:UNUSED_PAD src0_sel:WORD_1
	s_waitcnt lgkmcnt(1)
	v_max_f32_e32 v0, v0, v0
	s_waitcnt lgkmcnt(0)
	v_max_f32_e64 v4, |v4|, |v4|
	v_max_f32_e32 v0, v4, v0
	v_rcp_f32_e32 v0, v0
	v_max_f32_e32 v1, v1, v1
	v_max_f32_e64 v5, |v5|, |v5|
	v_max_f32_e32 v1, v5, v1
	v_fma_mixlo_f16 v4, v8, v0, 0
	v_rcp_f32_e32 v1, v1
	ds_write_b16 v32, v4 offset:18560
	v_fma_mixlo_f16 v4, v24, v0, 0
	ds_write_b16 v32, v4 offset:18624
	v_fma_mixlo_f16 v4, v40, v0, 0
	ds_write_b16 v32, v4 offset:18688
	v_fma_mixlo_f16 v0, v56, v0, 0
	v_max_f32_e32 v2, v2, v2
	v_max_f32_e64 v4, |v6|, |v6|
	ds_write_b16 v32, v0 offset:18752
	v_fma_mixlo_f16 v0, v9, v1, 0
	v_max_f32_e32 v2, v4, v2
	ds_write_b16 v186, v0 offset:21008
	v_fma_mixlo_f16 v0, v25, v1, 0
	v_rcp_f32_e32 v2, v2
	ds_write_b16 v186, v0 offset:21072
	v_fma_mixlo_f16 v0, v41, v1, 0
	ds_write_b16 v186, v0 offset:21136
	v_fma_mixlo_f16 v0, v57, v1, 0
	v_max_f32_e32 v1, v3, v3
	v_max_f32_e64 v3, |v7|, |v7|
	v_max_f32_e32 v1, v3, v1
	ds_write_b16 v186, v0 offset:21200
	v_fma_mixlo_f16 v0, v10, v2, 0
	v_rcp_f32_e32 v1, v1
	ds_write_b16 v186, v0 offset:21280
	v_fma_mixlo_f16 v0, v26, v2, 0
	ds_write_b16 v186, v0 offset:21344
	v_fma_mixlo_f16 v0, v42, v2, 0
	ds_write_b16 v186, v0 offset:21408
	v_fma_mixlo_f16 v0, v58, v2, 0
	ds_write_b16 v186, v0 offset:21472
	v_fma_mixlo_f16 v0, v11, v1, 0
	ds_write_b16 v186, v0 offset:21552
	v_fma_mixlo_f16 v0, v27, v1, 0
	ds_write_b16 v186, v0 offset:21616
	v_fma_mixlo_f16 v0, v43, v1, 0
	ds_write_b16 v186, v0 offset:21680
	v_fma_mixlo_f16 v0, v59, v1, 0
	ds_write_b16 v186, v0 offset:21744
	ds_read_b128 v[0:3], v188 offset:25952
	ds_read_b128 v[4:7], v188 offset:26208
	v_cvt_f32_f16_e32 v156, v157
	v_cvt_f32_f16_sdwa v157, v157 dst_sel:DWORD dst_unused:UNUSED_PAD src0_sel:WORD_1
	v_cvt_f32_f16_e32 v222, v151
	s_waitcnt lgkmcnt(1)
; __device__ __forceinline__ void x3_wave(int item, int b0, const h16* __restrict__ proj, const float* __restrict__ small, const h16* __restrict__ qkc, const h16* __restrict__ CS, ...
;     ...
;         for (int g = 0; g < 4; ++g) { const f32x4 dn = *(lds_cf32x4*)(R + W_SC + 1024 + (32 * tb + 8 * g + 4 * hi) * 4), em = *(lds_cf32x4*)(R + W_SC + 768 + (32 * tb + 8 * g + 4 * hi) * 4);
; #pragma unroll
;             for (int i = 0; i < 4; ++i) { const float inv = __builtin_amdgcn_rcpf(fmaxf(fabsf(dn[i]), em[i])); const int rl = 8 * g + 4 * hi + i;
; #pragma unroll
;                 for (int vb = 0; vb < 4; ++vb) *(__attribute__((address_space(3))) h16*)(R + W_K + rl * 272 + (32 * vb + r32) * 2) = (h16)(acc[vb][4 * g + i] * inv); } }
	v_max_f32_e32 v0, v0, v0
	s_waitcnt lgkmcnt(0)
	v_max_f32_e64 v4, |v4|, |v4|
	v_max_f32_e32 v0, v4, v0
	v_rcp_f32_e32 v0, v0
	v_max_f32_e32 v1, v1, v1
	v_max_f32_e64 v5, |v5|, |v5|
	v_max_f32_e32 v1, v5, v1
	v_fma_mixlo_f16 v4, v12, v0, 0
	ds_write_b16 v32, v4 offset:20736
	v_fma_mixlo_f16 v4, v28, v0, 0
	v_rcp_f32_e32 v1, v1
	ds_write_b16 v32, v4 offset:20800
	v_fma_mixlo_f16 v4, v44, v0, 0
	ds_write_b16 v32, v4 offset:20864
	v_max_f32_e32 v2, v2, v2
	v_max_f32_e64 v4, |v6|, |v6|
	v_fma_mixlo_f16 v0, v60, v0, 0
	v_max_f32_e32 v2, v4, v2
	ds_write_b16 v32, v0 offset:20928
	v_fma_mixlo_f16 v0, v13, v1, 0
	v_rcp_f32_e32 v2, v2
	ds_write_b16 v186, v0 offset:23184
	v_fma_mixlo_f16 v0, v29, v1, 0
	ds_write_b16 v186, v0 offset:23248
	v_fma_mixlo_f16 v0, v45, v1, 0
	ds_write_b16 v186, v0 offset:23312
	v_fma_mixlo_f16 v0, v61, v1, 0
	ds_write_b16 v186, v0 offset:23376
	v_fma_mixlo_f16 v0, v14, v2, 0
	ds_write_b16 v186, v0 offset:23456
	v_fma_mixlo_f16 v0, v30, v2, 0
	ds_write_b16 v186, v0 offset:23520
	v_fma_mixlo_f16 v0, v46, v2, 0
	ds_write_b16 v186, v0 offset:23584
	v_fma_mixlo_f16 v0, v62, v2, 0
	v_cvt_f32_f16_e32 v2, v174
	v_cvt_f32_f16_sdwa v4, v174 dst_sel:DWORD dst_unused:UNUSED_PAD src0_sel:WORD_1
	v_cvt_f32_f16_e32 v5, v175
	v_max_f32_e32 v1, v3, v3
	v_mul_f32_e32 v2, 0xbfb8aa3b, v2
	v_exp_f32_e32 v2, v2
	v_max_f32_e64 v3, |v7|, |v7|
	v_max_f32_e32 v1, v3, v1
	v_mul_f32_e32 v4, 0xbfb8aa3b, v4
	v_add_f32_e32 v2, 1.0, v2
	v_rcp_f32_e32 v1, v1
	v_exp_f32_e32 v4, v4
	v_rcp_f32_e32 v30, v2
	v_mul_f32_e32 v2, 0xbfb8aa3b, v5
	v_cvt_f32_f16_sdwa v5, v175 dst_sel:DWORD dst_unused:UNUSED_PAD src0_sel:WORD_1
	ds_write_b16 v186, v0 offset:23648
	v_fma_mixlo_f16 v0, v15, v1, 0
	v_exp_f32_e32 v2, v2
	v_add_f32_e32 v4, 1.0, v4
	v_mul_f32_e32 v5, 0xbfb8aa3b, v5
	ds_write_b16 v186, v0 offset:23728
	v_fma_mixlo_f16 v0, v31, v1, 0
	v_rcp_f32_e32 v31, v4
	v_cvt_f32_f16_e32 v4, v176
	v_exp_f32_e32 v5, v5
	v_add_f32_e32 v2, 1.0, v2
	v_rcp_f32_e32 v34, v2
	v_mul_f32_e32 v2, 0xbfb8aa3b, v4
	v_add_f32_e32 v4, 1.0, v5
	v_cvt_f32_f16_sdwa v5, v176 dst_sel:DWORD dst_unused:UNUSED_PAD src0_sel:WORD_1
	v_exp_f32_e32 v2, v2
	v_rcp_f32_e32 v35, v4
	v_cvt_f32_f16_e32 v4, v177
	v_mul_f32_e32 v5, 0xbfb8aa3b, v5
	v_exp_f32_e32 v5, v5
	v_add_f32_e32 v2, 1.0, v2
	v_rcp_f32_e32 v58, v2
	v_mul_f32_e32 v2, 0xbfb8aa3b, v4
	v_add_f32_e32 v4, 1.0, v5
	v_cvt_f32_f16_sdwa v5, v177 dst_sel:DWORD dst_unused:UNUSED_PAD src0_sel:WORD_1
	v_exp_f32_e32 v2, v2
	v_rcp_f32_e32 v59, v4
	v_cvt_f32_f16_e32 v4, v170
	v_mul_f32_e32 v5, 0xbfb8aa3b, v5
	v_exp_f32_e32 v5, v5
	v_add_f32_e32 v2, 1.0, v2
	v_rcp_f32_e32 v48, v2
	v_mul_f32_e32 v2, 0xbfb8aa3b, v4
	v_add_f32_e32 v4, 1.0, v5
	v_cvt_f32_f16_sdwa v5, v170 dst_sel:DWORD dst_unused:UNUSED_PAD src0_sel:WORD_1
	v_exp_f32_e32 v2, v2
	v_rcp_f32_e32 v49, v4
	v_cvt_f32_f16_e32 v4, v171
	v_mul_f32_e32 v5, 0xbfb8aa3b, v5
	v_exp_f32_e32 v5, v5
	v_add_f32_e32 v2, 1.0, v2
	v_rcp_f32_e32 v26, v2
	v_mul_f32_e32 v2, 0xbfb8aa3b, v4
	v_add_f32_e32 v4, 1.0, v5
	v_cvt_f32_f16_sdwa v5, v171 dst_sel:DWORD dst_unused:UNUSED_PAD src0_sel:WORD_1
	v_exp_f32_e32 v2, v2
	v_rcp_f32_e32 v27, v4
	v_cvt_f32_f16_e32 v4, v172
	v_mul_f32_e32 v5, 0xbfb8aa3b, v5
	v_exp_f32_e32 v5, v5
	v_add_f32_e32 v2, 1.0, v2
	v_rcp_f32_e32 v28, v2
	v_mul_f32_e32 v2, 0xbfb8aa3b, v4
	v_add_f32_e32 v4, 1.0, v5
	v_cvt_f32_f16_sdwa v5, v172 dst_sel:DWORD dst_unused:UNUSED_PAD src0_sel:WORD_1
	v_exp_f32_e32 v2, v2
	v_rcp_f32_e32 v29, v4
	v_cvt_f32_f16_e32 v4, v173
	v_mul_f32_e32 v5, 0xbfb8aa3b, v5
	v_exp_f32_e32 v5, v5
	v_add_f32_e32 v2, 1.0, v2
	v_rcp_f32_e32 v32, v2
	v_mul_f32_e32 v2, 0xbfb8aa3b, v4
	v_add_f32_e32 v4, 1.0, v5
	v_cvt_f32_f16_sdwa v5, v173 dst_sel:DWORD dst_unused:UNUSED_PAD src0_sel:WORD_1
	v_exp_f32_e32 v2, v2
	v_rcp_f32_e32 v33, v4
	v_cvt_f32_f16_e32 v4, v166
	v_mul_f32_e32 v5, 0xbfb8aa3b, v5
	v_exp_f32_e32 v5, v5
	v_add_f32_e32 v2, 1.0, v2
	v_rcp_f32_e32 v36, v2
	v_mul_f32_e32 v2, 0xbfb8aa3b, v4
	v_add_f32_e32 v4, 1.0, v5
	v_cvt_f32_f16_sdwa v5, v166 dst_sel:DWORD dst_unused:UNUSED_PAD src0_sel:WORD_1
	v_exp_f32_e32 v2, v2
	v_rcp_f32_e32 v37, v4
	v_cvt_f32_f16_e32 v4, v167
	v_mul_f32_e32 v5, 0xbfb8aa3b, v5
	v_exp_f32_e32 v5, v5
	v_add_f32_e32 v2, 1.0, v2
	v_rcp_f32_e32 v44, v2
	v_mul_f32_e32 v2, 0xbfb8aa3b, v4
	v_exp_f32_e32 v2, v2
	v_add_f32_e32 v4, 1.0, v5
	v_rcp_f32_e32 v45, v4
	v_cvt_f32_f16_sdwa v4, v167 dst_sel:DWORD dst_unused:UNUSED_PAD src0_sel:WORD_1
	v_cvt_f32_f16_e32 v5, v168
	v_add_f32_e32 v2, 1.0, v2
	v_rcp_f32_e32 v60, v2
	v_mul_f32_e32 v2, 0xbfb8aa3b, v4
	v_exp_f32_e32 v2, v2
	v_mul_f32_e32 v4, 0xbfb8aa3b, v5
	v_exp_f32_e32 v4, v4
	v_cvt_f32_f16_sdwa v5, v168 dst_sel:DWORD dst_unused:UNUSED_PAD src0_sel:WORD_1
	v_add_f32_e32 v2, 1.0, v2
	v_rcp_f32_e32 v61, v2
	v_add_f32_e32 v2, 1.0, v4
	v_mul_f32_e32 v4, 0xbfb8aa3b, v5
	v_cvt_f32_f16_e32 v5, v169
	v_exp_f32_e32 v4, v4
	v_rcp_f32_e32 v168, v2
	v_cvt_f32_f16_sdwa v2, v169 dst_sel:DWORD dst_unused:UNUSED_PAD src0_sel:WORD_1
	v_mul_f32_e32 v5, 0xbfb8aa3b, v5
	v_exp_f32_e32 v5, v5
	ds_write_b16 v186, v0 offset:23792
	v_fma_mixlo_f16 v0, v47, v1, 0
	v_add_f32_e32 v4, 1.0, v4
	v_mul_f32_e32 v2, 0xbfb8aa3b, v2
	ds_write_b16 v186, v0 offset:23856
	v_fma_mixlo_f16 v0, v63, v1, 0
	v_exp_f32_e32 v2, v2
	v_rcp_f32_e32 v169, v4
	v_add_f32_e32 v4, 1.0, v5
	ds_write_b16 v186, v0 offset:23920
	v_mov_b32_e32 v1, v250
	v_rcp_f32_e32 v178, v4
	v_cvt_f32_f16_e32 v4, v162
	s_waitcnt lgkmcnt(0)
	v_add_f32_e32 v2, 1.0, v2
	v_ashrrev_i32_e32 v0, 2, v1
	v_lshlrev_b32_e32 v1, 5, v1
	v_and_b32_e32 v12, 0x60, v1
	v_mul_lo_u32 v3, v0, s44
	v_lshlrev_b32_e32 v96, 1, v12
	v_rcp_f32_e32 v179, v2
	v_mul_f32_e32 v2, 0xbfb8aa3b, v4
	v_add3_u32 v3, s5, v3, v96
	v_exp_f32_e32 v2, v2
	ds_read_b128 v[174:177], v3 offset:16384
	ds_read_b128 v[22:25], v3 offset:16400
	v_cvt_f32_f16_sdwa v4, v162 dst_sel:DWORD dst_unused:UNUSED_PAD src0_sel:WORD_1
	ds_read_b128 v[18:21], v3 offset:16416
	ds_read_b128 v[8:11], v3 offset:16432
	v_cvt_f32_f16_e32 v3, v163
	v_add_f32_e32 v2, 1.0, v2
	v_mul_f32_e32 v4, 0xbfb8aa3b, v4
	v_rcp_f32_e32 v46, v2
	v_mul_f32_e32 v2, 0xbfb8aa3b, v3
	v_exp_f32_e32 v4, v4
	v_exp_f32_e32 v2, v2
	v_cvt_f32_f16_e32 v5, v165
	v_cvt_f32_f16_sdwa v6, v165 dst_sel:DWORD dst_unused:UNUSED_PAD src0_sel:WORD_1
	v_add_f32_e32 v3, 1.0, v4
	v_add_f32_e32 v2, 1.0, v2
	v_rcp_f32_e32 v47, v3
	v_cvt_f32_f16_sdwa v3, v163 dst_sel:DWORD dst_unused:UNUSED_PAD src0_sel:WORD_1
	v_rcp_f32_e32 v50, v2
	v_cvt_f32_f16_e32 v2, v164
	v_cvt_f32_f16_sdwa v4, v164 dst_sel:DWORD dst_unused:UNUSED_PAD src0_sel:WORD_1
	v_mul_f32_e32 v3, 0xbfb8aa3b, v3
	v_exp_f32_e32 v3, v3
	v_mul_f32_e32 v2, 0xbfb8aa3b, v2
	v_mul_f32_e32 v4, 0xbfb8aa3b, v4
	v_exp_f32_e32 v2, v2
	v_exp_f32_e32 v4, v4
	v_mul_f32_e32 v5, 0xbfb8aa3b, v5
	v_add_f32_e32 v13, 1.0, v3
	v_add_f32_e32 v2, 1.0, v2
	v_add_f32_e32 v3, 1.0, v4
	v_exp_f32_e32 v7, v5
	v_mul_f32_e32 v5, 0xbfb8aa3b, v6
	v_rcp_f32_e32 v2, v2
	v_rcp_f32_e32 v3, v3
	s_waitcnt lgkmcnt(0)
	v_cvt_f32_f16_e32 v4, v10
	v_exp_f32_e32 v14, v5
	v_cvt_f32_f16_sdwa v5, v10 dst_sel:DWORD dst_unused:UNUSED_PAD src0_sel:WORD_1
	v_cvt_f32_f16_e32 v164, v175
	v_cvt_f32_f16_sdwa v165, v175 dst_sel:DWORD dst_unused:UNUSED_PAD src0_sel:WORD_1
	v_cvt_f32_f16_sdwa v163, v159 dst_sel:DWORD dst_unused:UNUSED_PAD src0_sel:WORD_1
	v_cvt_f32_f16_e32 v162, v159
	v_ashrrev_i32_e32 v1, 31, v0
	v_pk_mul_f32 v[42:43], v[2:3], v[4:5]
	v_lshl_add_u64 v[0:1], s[42:43], 0, v[0:1]
	v_mov_b64_e32 v[2:3], s[20:21]
	v_pk_mul_f32 v[164:165], v[34:35], v[164:165]
	v_mul_f32_e32 v35, 0xbfb8aa3b, v163
	v_mad_u64_u32 v[2:3], s[10:11], v0, s7, v[2:3]
	v_mul_f32_e32 v34, 0xbfb8aa3b, v162
	v_exp_f32_e32 v35, v35
	v_mov_b32_e32 v0, v3
	v_exp_f32_e32 v34, v34
	v_cvt_f32_f16_e32 v172, v158
	v_mad_u64_u32 v[0:1], s[10:11], v1, s7, v[0:1]
	v_mov_b32_e32 v3, v0
	v_lshl_add_u64 v[40:41], v[2:3], 0, v[96:97]
	v_add_f32_e32 v96, 1.0, v35
	v_add_f32_e32 v34, 1.0, v34
	v_rcp_f32_e32 v167, v96
	v_mul_f32_e32 v96, 0xbfb8aa3b, v172
	v_rcp_f32_e32 v166, v34
	v_cvt_f32_f16_e32 v34, v174
	v_cvt_f32_f16_sdwa v35, v174 dst_sel:DWORD dst_unused:UNUSED_PAD src0_sel:WORD_1
	v_exp_f32_e32 v96, v96
	v_cvt_f32_f16_sdwa v173, v158 dst_sel:DWORD dst_unused:UNUSED_PAD src0_sel:WORD_1
	v_cvt_f32_f16_e32 v158, v161
	v_pk_mul_f32 v[174:175], v[30:31], v[34:35]
	v_add_f32_e32 v30, 1.0, v96
	v_rcp_f32_e32 v180, v30
	v_mul_f32_e32 v30, 0xbfb8aa3b, v173
	v_exp_f32_e32 v30, v30
	v_mul_f32_e32 v31, 0xbfb8aa3b, v158
	v_cvt_f32_f16_sdwa v159, v161 dst_sel:DWORD dst_unused:UNUSED_PAD src0_sel:WORD_1
	v_exp_f32_e32 v31, v31
	v_add_f32_e32 v30, 1.0, v30
	v_rcp_f32_e32 v181, v30
	v_mul_f32_e32 v30, 0xbfb8aa3b, v159
	v_cvt_f32_f16_e32 v56, v177
	v_cvt_f32_f16_sdwa v57, v177 dst_sel:DWORD dst_unused:UNUSED_PAD src0_sel:WORD_1
	v_add_f32_e32 v34, 1.0, v31
	v_exp_f32_e32 v35, v30
	v_cvt_f32_f16_e32 v30, v25
	v_cvt_f32_f16_sdwa v31, v25 dst_sel:DWORD dst_unused:UNUSED_PAD src0_sel:WORD_1
	v_pk_mul_f32 v[48:49], v[48:49], v[56:57]
	v_cvt_f32_f16_e32 v56, v160
	v_cvt_f32_f16_sdwa v57, v160 dst_sel:DWORD dst_unused:UNUSED_PAD src0_sel:WORD_1
	v_add_f32_e32 v25, 1.0, v35
	v_pk_mul_f32 v[160:161], v[36:37], v[30:31]
	v_cvt_f32_f16_e32 v30, v24
	v_cvt_f32_f16_sdwa v31, v24 dst_sel:DWORD dst_unused:UNUSED_PAD src0_sel:WORD_1
	v_mul_f32_e32 v24, 0xbfb8aa3b, v182
	v_rcp_f32_e32 v185, v25
	v_exp_f32_e32 v24, v24
	v_mul_f32_e32 v25, 0xbfb8aa3b, v183
	v_exp_f32_e32 v25, v25
	v_add_f32_e32 v6, 1.0, v7
	v_add_f32_e32 v7, 1.0, v14
	v_add_f32_e32 v24, 1.0, v24
	v_rcp_f32_e32 v6, v6
	v_rcp_f32_e32 v7, v7
	v_cvt_f32_f16_e32 v10, v11
	v_cvt_f32_f16_sdwa v11, v11 dst_sel:DWORD dst_unused:UNUSED_PAD src0_sel:WORD_1
	v_pk_mul_f32 v[186:187], v[32:33], v[30:31]
	v_rcp_f32_e32 v190, v24
	v_add_f32_e32 v30, 1.0, v25
	v_cvt_f32_f16_e32 v24, v23
	v_cvt_f32_f16_sdwa v25, v23 dst_sel:DWORD dst_unused:UNUSED_PAD src0_sel:WORD_1
	v_lshlrev_b32_e32 v216, 2, v12
	v_mul_f32_e32 v23, 0xbfb8aa3b, v192
	v_rcp_f32_e32 v51, v13
	v_pk_mul_f32 v[38:39], v[6:7], v[10:11]
	global_load_dwordx4 v[0:3], v216, s[14:15] offset:48
	global_load_dwordx4 v[4:7], v216, s[14:15] offset:32
	global_load_dwordx4 v[10:13], v216, s[14:15] offset:16
	global_load_dwordx4 v[14:17], v216, s[14:15]
	v_pk_mul_f32 v[196:197], v[28:29], v[24:25]
	v_exp_f32_e32 v23, v23
	v_mul_f32_e32 v24, 0xbfb8aa3b, v193
	v_exp_f32_e32 v24, v24
	v_cvt_f32_f16_sdwa v25, v22 dst_sel:DWORD dst_unused:UNUSED_PAD src0_sel:WORD_1
	v_add_f32_e32 v23, 1.0, v23
	v_rcp_f32_e32 v198, v23
	v_add_f32_e32 v23, 1.0, v24
	v_cvt_f32_f16_e32 v24, v22
	v_mul_f32_e32 v22, 0xbfb8aa3b, v200
	v_rcp_f32_e32 v199, v23
	v_exp_f32_e32 v22, v22
	v_mul_f32_e32 v23, 0xbfb8aa3b, v201
	v_exp_f32_e32 v23, v23
	v_pk_mul_f32 v[154:155], v[26:27], v[24:25]
	v_add_f32_e32 v22, 1.0, v22
	v_rcp_f32_e32 v204, v22
	v_add_f32_e32 v22, 1.0, v23
	v_mul_f32_e32 v23, 0xbfb8aa3b, v156
	v_exp_f32_e32 v23, v23
	v_mul_f32_e32 v24, 0xbfb8aa3b, v157
	v_exp_f32_e32 v24, v24
	v_rcp_f32_e32 v205, v22
	v_add_f32_e32 v22, 1.0, v23
	v_rcp_f32_e32 v206, v22
	v_add_f32_e32 v22, 1.0, v24
	v_rcp_f32_e32 v184, v34
	v_rcp_f32_e32 v191, v30
	v_rcp_f32_e32 v207, v22
	global_load_dwordx4 v[22:25], v216, s[14:15] offset:112
	global_load_dwordx4 v[26:29], v216, s[14:15] offset:96
	global_load_dwordx4 v[30:33], v216, s[14:15] offset:80
	global_load_dwordx4 v[34:37], v216, s[14:15] offset:64
	v_cvt_f32_f16_e32 v214, v21
	v_cvt_f32_f16_sdwa v215, v21 dst_sel:DWORD dst_unused:UNUSED_PAD src0_sel:WORD_1
	v_cvt_f32_f16_e32 v62, v176
	v_cvt_f32_f16_sdwa v63, v176 dst_sel:DWORD dst_unused:UNUSED_PAD src0_sel:WORD_1
	v_cvt_f32_f16_sdwa v21, v152 dst_sel:DWORD dst_unused:UNUSED_PAD src0_sel:WORD_1
	v_pk_mul_f32 v[178:179], v[178:179], v[214:215]
	v_cvt_f32_f16_e32 v214, v20
	v_cvt_f32_f16_sdwa v215, v20 dst_sel:DWORD dst_unused:UNUSED_PAD src0_sel:WORD_1
	v_cvt_f32_f16_e32 v20, v152
	v_pk_mul_f32 v[194:195], v[174:175], v[174:175]
	v_pk_mul_f32 v[188:189], v[164:165], v[164:165]
	v_add_f32_e32 v194, v194, v195
	v_mul_f32_e32 v96, 0xbfb8aa3b, v20
	v_pk_mul_f32 v[58:59], v[58:59], v[62:63]
	v_exp_f32_e32 v96, v96
	v_mul_f32_e32 v152, 0xbfb8aa3b, v21
	v_add_f32_e32 v188, v188, v194
	v_pk_mul_f32 v[176:177], v[58:59], v[58:59]
	v_exp_f32_e32 v152, v152
	v_add_f32_e32 v188, v189, v188
	v_cvt_f32_f16_sdwa v223, v151 dst_sel:DWORD dst_unused:UNUSED_PAD src0_sel:WORD_1
	v_add_f32_e32 v176, v176, v188
	v_pk_mul_f32 v[170:171], v[48:49], v[48:49]
	v_add_f32_e32 v176, v177, v176
	v_add_f32_e32 v96, 1.0, v96
	v_add_f32_e32 v170, v170, v176
	v_pk_mul_f32 v[212:213], v[154:155], v[154:155]
	v_rcp_f32_e32 v218, v96
	v_add_f32_e32 v96, 1.0, v152
	v_cvt_f32_f16_e32 v220, v19
	v_cvt_f32_f16_sdwa v221, v19 dst_sel:DWORD dst_unused:UNUSED_PAD src0_sel:WORD_1
	v_mul_f32_e32 v19, 0xbfb8aa3b, v222
	v_add_f32_e32 v170, v171, v170
	v_rcp_f32_e32 v219, v96
	v_exp_f32_e32 v19, v19
	v_mul_f32_e32 v96, 0xbfb8aa3b, v223
	v_add_f32_e32 v170, v212, v170
	v_pk_mul_f32 v[210:211], v[196:197], v[196:197]
	v_exp_f32_e32 v96, v96
	v_cvt_f32_f16_e32 v226, v150
	v_add_f32_e32 v170, v213, v170
	v_cvt_f32_f16_e32 v228, v18
	v_cvt_f32_f16_sdwa v229, v18 dst_sel:DWORD dst_unused:UNUSED_PAD src0_sel:WORD_1
	v_add_f32_e32 v170, v210, v170
	v_pk_mul_f32 v[208:209], v[186:187], v[186:187]
	v_add_f32_e32 v170, v211, v170
	v_add_f32_e32 v19, 1.0, v19
	v_add_f32_e32 v170, v208, v170
	v_pk_mul_f32 v[202:203], v[160:161], v[160:161]
	v_rcp_f32_e32 v224, v19
	v_add_f32_e32 v19, 1.0, v96
	v_mul_f32_e32 v18, 0xbfb8aa3b, v226
	v_add_f32_e32 v170, v209, v170
	v_rcp_f32_e32 v225, v19
	v_exp_f32_e32 v96, v18
	v_pk_mul_f32 v[18:19], v[44:45], v[228:229]
	v_add_f32_e32 v170, v202, v170
	v_pk_mul_f32 v[44:45], v[18:19], v[18:19]
	v_add_f32_e32 v170, v203, v170
	v_pk_mul_f32 v[60:61], v[60:61], v[220:221]
	v_add_f32_e32 v44, v44, v170
	v_pk_mul_f32 v[220:221], v[60:61], v[60:61]
	v_add_f32_e32 v44, v45, v44
	v_pk_mul_f32 v[168:169], v[168:169], v[214:215]
	v_cvt_f32_f16_e32 v234, v8
	v_cvt_f32_f16_sdwa v235, v8 dst_sel:DWORD dst_unused:UNUSED_PAD src0_sel:WORD_1
	v_add_f32_e32 v44, v220, v44
	v_pk_mul_f32 v[214:215], v[168:169], v[168:169]
	v_cvt_f32_f16_e32 v232, v9
	v_cvt_f32_f16_sdwa v233, v9 dst_sel:DWORD dst_unused:UNUSED_PAD src0_sel:WORD_1
	v_add_f32_e32 v44, v221, v44
	v_add_f32_e32 v44, v214, v44
	v_pk_mul_f32 v[216:217], v[178:179], v[178:179]
	v_add_f32_e32 v44, v215, v44
	v_pk_mul_f32 v[46:47], v[46:47], v[234:235]
	v_add_f32_e32 v44, v216, v44
	v_pk_mul_f32 v[50:51], v[50:51], v[232:233]
	v_pk_mul_f32 v[232:233], v[46:47], v[46:47]
	v_add_f32_e32 v44, v217, v44
	v_add_f32_e32 v44, v232, v44
	v_pk_mul_f32 v[8:9], v[50:51], v[50:51]
	v_add_f32_e32 v44, v233, v44
	v_cvt_f32_f16_sdwa v227, v150 dst_sel:DWORD dst_unused:UNUSED_PAD src0_sel:WORD_1
	v_add_f32_e32 v8, v8, v44
	v_pk_mul_f32 v[52:53], v[42:43], v[42:43]
	v_add_f32_e32 v8, v9, v8
	v_add_f32_e32 v8, v52, v8
	v_pk_mul_f32 v[54:55], v[38:39], v[38:39]
	v_cvt_f32_f16_e32 v150, v153
	v_add_f32_e32 v8, v53, v8
	v_mul_f32_e32 v151, 0xbfb8aa3b, v227
	v_add_f32_e32 v8, v54, v8
	v_exp_f32_e32 v151, v151
	v_add_f32_e32 v8, v55, v8
	v_add_f32_e32 v96, 1.0, v96
	ds_swizzle_b32 v9, v8 offset:swizzle(SWAP,1)
	v_rcp_f32_e32 v152, v96
	v_mul_f32_e32 v96, 0xbfb8aa3b, v150
	v_exp_f32_e32 v96, v96
	v_add_f32_e32 v228, 1.0, v151
	v_cvt_f32_f16_sdwa v151, v153 dst_sel:DWORD dst_unused:UNUSED_PAD src0_sel:WORD_1
	v_cvt_f32_f16_e32 v234, v146
	s_waitcnt lgkmcnt(0)
	v_add_f32_e32 v8, v8, v9
	v_add_f32_e32 v96, 1.0, v96
	ds_swizzle_b32 v9, v8 offset:swizzle(SWAP,2)
	v_rcp_f32_e32 v153, v228
	v_rcp_f32_e32 v228, v96
	v_mul_f32_e32 v96, 0xbfb8aa3b, v151
	v_exp_f32_e32 v96, v96
	v_mul_f32_e32 v45, 0xbfb8aa3b, v234
	v_cvt_f32_f16_sdwa v235, v146 dst_sel:DWORD dst_unused:UNUSED_PAD src0_sel:WORD_1
	v_exp_f32_e32 v45, v45
	s_waitcnt lgkmcnt(0)
	v_add_f32_e32 v8, v8, v9
	v_add_f32_e32 v44, 1.0, v96
	v_fmamk_f32 v8, v8, 0x3c000000, v242
	v_rcp_f32_e32 v229, v44
	v_add_f32_e32 v44, 1.0, v45
	v_mul_f32_e32 v45, 0xbfb8aa3b, v235
	v_mul_f32_e32 v9, 0x4b800000, v8
	v_cmp_gt_f32_e32 vcc, s34, v8
	v_exp_f32_e32 v45, v45
	v_mul_f32_e32 v62, 0xbfb8aa3b, v56
	v_cndmask_b32_e32 v8, v8, v9, vcc
	v_rsq_f32_e32 v8, v8
	v_mul_f32_e32 v63, 0xbfb8aa3b, v57
	v_exp_f32_e32 v62, v62
	v_exp_f32_e32 v63, v63
	v_add_f32_e32 v9, 1.0, v45
	v_rcp_f32_e32 v45, v9
	v_mul_f32_e32 v9, 0x45800000, v8
	v_cndmask_b32_e32 v52, v8, v9, vcc
	v_pk_mul_f32 v[8:9], v[174:175], v[52:53] op_sel_hi:[1,0]
	v_add_f32_e32 v62, 1.0, v62
	v_add_f32_e32 v63, 1.0, v63
	s_waitcnt vmcnt(4)
; __device__ __forceinline__ void x3_wave(int item, int b0, const h16* __restrict__ proj, const float* __restrict__ small, const h16* __restrict__ qkc, const h16* __restrict__ CS, ...
;     ...
;         if (tb == 0) { int l4 = threadIdx.x & 63; asm volatile("" : "+v"(l4)); const int r32b = l4 & 31, hib = l4 >> 5;
; #pragma unroll
;             for (int ks = 0; ks < 4; ++ks) { qr[ks] = *(const s16x8*)(qkc + (row0 + 32 + r32b) * 512 + hh * 64 + 16 * ks + 8 * hib);
;                 kB[ks] = *(const s16x8*)(qkc + (row0 + 32 + r32b) * 512 + 256 + hh * 64 + 16 * ks + 8 * hib); } }
	v_pk_mul_f32 v[8:9], v[14:15], v[8:9]
	v_pk_mul_f32 v[14:15], v[164:165], v[52:53] op_sel_hi:[1,0]
	v_rcp_f32_e32 v62, v62
	v_rcp_f32_e32 v63, v63
	v_pk_mul_f32 v[14:15], v[16:17], v[14:15]
	v_pk_mul_f32 v[16:17], v[58:59], v[52:53] op_sel_hi:[1,0]
	v_pk_mul_f32 v[8:9], v[8:9], v[172:173]
	v_pk_mul_f32 v[10:11], v[10:11], v[16:17]
	v_pk_mul_f32 v[16:17], v[48:49], v[52:53] op_sel_hi:[1,0]
	v_pk_mul_f32 v[14:15], v[14:15], v[162:163]
	v_pk_mul_f32 v[12:13], v[12:13], v[16:17]
	v_pk_mul_f32 v[10:11], v[10:11], v[56:57]
	v_pk_mul_f32 v[12:13], v[12:13], v[158:159]
	v_pk_mul_f32 v[8:9], v[180:181], v[8:9]
	v_pk_mul_f32 v[14:15], v[166:167], v[14:15]
	v_pk_mul_f32 v[10:11], v[62:63], v[10:11]
	v_pk_mul_f32 v[12:13], v[184:185], v[12:13]
	v_cvt_pk_f16_f32 v8, v8, v9
	v_cvt_pk_f16_f32 v9, v14, v15
	v_cvt_pk_f16_f32 v10, v10, v11
	v_cvt_pk_f16_f32 v11, v12, v13
	global_store_dwordx4 v[40:41], v[8:11], off offset:2048 sc1
	v_rcp_f32_e32 v44, v44
	s_andn2_b64 vcc, exec, s[46:47]
	v_pk_mul_f32 v[8:9], v[154:155], v[52:53] op_sel_hi:[1,0]
	s_nop 0
	v_pk_mul_f32 v[4:5], v[4:5], v[8:9]
	v_pk_mul_f32 v[8:9], v[196:197], v[52:53] op_sel_hi:[1,0]
	v_pk_mul_f32 v[4:5], v[4:5], v[200:201]
	v_pk_mul_f32 v[6:7], v[6:7], v[8:9]
	v_pk_mul_f32 v[8:9], v[186:187], v[52:53] op_sel_hi:[1,0]
	v_pk_mul_f32 v[6:7], v[6:7], v[192:193]
	v_pk_mul_f32 v[0:1], v[0:1], v[8:9]
	v_pk_mul_f32 v[4:5], v[204:205], v[4:5]
	v_pk_mul_f32 v[0:1], v[0:1], v[182:183]
	v_pk_mul_f32 v[6:7], v[198:199], v[6:7]
	v_pk_mul_f32 v[8:9], v[190:191], v[0:1]
	v_pk_mul_f32 v[0:1], v[160:161], v[52:53] op_sel_hi:[1,0]
	s_nop 0
	v_pk_mul_f32 v[0:1], v[2:3], v[0:1]
	v_cvt_pk_f16_f32 v2, v8, v9
	v_pk_mul_f32 v[0:1], v[0:1], v[156:157]
	v_cvt_f32_f16_e32 v8, v148
	v_pk_mul_f32 v[10:11], v[206:207], v[0:1]
	v_cvt_pk_f16_f32 v0, v4, v5
	v_cvt_pk_f16_f32 v1, v6, v7
	v_cvt_pk_f16_f32 v3, v10, v11
	global_store_dwordx4 v[40:41], v[0:3], off offset:2064 sc1
	v_pk_mul_f32 v[4:5], v[168:169], v[52:53] op_sel_hi:[1,0]
	v_pk_mul_f32 v[6:7], v[178:179], v[52:53] op_sel_hi:[1,0]
	v_pk_mul_f32 v[0:1], v[18:19], v[52:53] op_sel_hi:[1,0]
	v_pk_mul_f32 v[2:3], v[60:61], v[52:53] op_sel_hi:[1,0]
	s_waitcnt vmcnt(2)
	v_pk_mul_f32 v[0:1], v[34:35], v[0:1]
	v_pk_mul_f32 v[2:3], v[36:37], v[2:3]
	v_pk_mul_f32 v[4:5], v[30:31], v[4:5]
	v_pk_mul_f32 v[0:1], v[0:1], v[226:227]
	v_pk_mul_f32 v[2:3], v[2:3], v[222:223]
	v_pk_mul_f32 v[4:5], v[4:5], v[20:21]
	v_pk_mul_f32 v[0:1], v[152:153], v[0:1]
	v_pk_mul_f32 v[2:3], v[224:225], v[2:3]
	v_pk_mul_f32 v[4:5], v[218:219], v[4:5]
	v_pk_mul_f32 v[6:7], v[32:33], v[6:7]
	v_cvt_pk_f16_f32 v0, v0, v1
	v_cvt_pk_f16_f32 v1, v2, v3
	v_cvt_pk_f16_f32 v2, v4, v5
	v_cvt_f32_f16_e32 v4, v147
	v_cvt_f32_f16_sdwa v5, v147 dst_sel:DWORD dst_unused:UNUSED_PAD src0_sel:WORD_1
	v_pk_mul_f32 v[6:7], v[6:7], v[150:151]
	v_mul_f32_e32 v9, 0xbfb8aa3b, v8
	v_pk_mul_f32 v[6:7], v[228:229], v[6:7]
	v_exp_f32_e32 v10, v9
	v_cvt_pk_f16_f32 v3, v6, v7
	global_store_dwordx4 v[40:41], v[0:3], off offset:2080 sc1
	v_cvt_f32_f16_sdwa v9, v148 dst_sel:DWORD dst_unused:UNUSED_PAD src0_sel:WORD_1
	v_pk_mul_f32 v[6:7], v[50:51], v[52:53] op_sel_hi:[1,0]
	v_mul_f32_e32 v2, 0xbfb8aa3b, v4
	v_mul_f32_e32 v3, 0xbfb8aa3b, v5
	v_exp_f32_e32 v2, v2
	v_exp_f32_e32 v3, v3
	v_pk_mul_f32 v[6:7], v[28:29], v[6:7]
	v_pk_mul_f32 v[0:1], v[46:47], v[52:53] op_sel_hi:[1,0]
	v_add_f32_e32 v2, 1.0, v2
	v_add_f32_e32 v3, 1.0, v3
	v_rcp_f32_e32 v2, v2
	v_rcp_f32_e32 v3, v3
	v_pk_mul_f32 v[4:5], v[6:7], v[4:5]
	v_pk_mul_f32 v[6:7], v[42:43], v[52:53] op_sel_hi:[1,0]
	v_pk_mul_f32 v[0:1], v[26:27], v[0:1]
	v_pk_mul_f32 v[2:3], v[2:3], v[4:5]
	v_mul_f32_e32 v5, 0xbfb8aa3b, v9
	v_pk_mul_f32 v[6:7], v[22:23], v[6:7]
	v_exp_f32_e32 v5, v5
	v_pk_mul_f32 v[6:7], v[6:7], v[8:9]
	v_cvt_f32_f16_e32 v8, v149
	v_cvt_f32_f16_sdwa v9, v149 dst_sel:DWORD dst_unused:UNUSED_PAD src0_sel:WORD_1
	v_add_f32_e32 v4, 1.0, v10
	v_add_f32_e32 v5, 1.0, v5
	v_mul_f32_e32 v10, 0xbfb8aa3b, v8
	v_mul_f32_e32 v11, 0xbfb8aa3b, v9
	v_rcp_f32_e32 v4, v4
	v_rcp_f32_e32 v5, v5
	v_exp_f32_e32 v10, v10
	v_exp_f32_e32 v11, v11
	v_pk_mul_f32 v[0:1], v[0:1], v[234:235]
	v_pk_mul_f32 v[4:5], v[4:5], v[6:7]
	v_add_f32_e32 v6, 1.0, v10
	v_add_f32_e32 v7, 1.0, v11
	v_rcp_f32_e32 v6, v6
	v_rcp_f32_e32 v7, v7
	v_pk_mul_f32 v[10:11], v[38:39], v[52:53] op_sel_hi:[1,0]
	v_pk_mul_f32 v[0:1], v[44:45], v[0:1]
	v_pk_mul_f32 v[10:11], v[24:25], v[10:11]
	v_cvt_pk_f16_f32 v0, v0, v1
	v_pk_mul_f32 v[8:9], v[10:11], v[8:9]
	v_cvt_pk_f16_f32 v1, v2, v3
	v_pk_mul_f32 v[6:7], v[6:7], v[8:9]
	v_cvt_pk_f16_f32 v2, v4, v5
	v_cvt_pk_f16_f32 v3, v6, v7
	global_store_dwordx4 v[40:41], v[0:3], off offset:2096 sc1
	s_cbranch_vccnz .LBB0_430
	s_nop 0
	v_mov_b32_e32 v2, v250
	v_mov_b32_e32 v1, s3
	v_and_or_b32 v0, v2, 31, s2
	v_lshlrev_b64 v[0:1], 10, v[0:1]
	v_ashrrev_i32_e32 v2, 2, v2
	v_lshl_add_u64 v[0:1], s[88:89], 0, v[0:1]
	s_mov_b32 s41, s29
	v_and_b32_e32 v2, -8, v2
	v_ashrrev_i32_e32 v3, 31, v2
	v_lshl_add_u64 v[0:1], v[0:1], 0, s[40:41]
	v_lshl_add_u64 v[0:1], v[2:3], 1, v[0:1]
	s_mov_b64 s[10:11], 0x8000
	v_lshl_add_u64 v[2:3], v[0:1], 0, s[10:11]
	s_mov_b64 s[10:11], 0x8200
	v_lshl_add_u64 v[4:5], v[0:1], 0, s[10:11]
	v_add_co_u32_e32 v0, vcc, 0x8000, v0
	s_nop 1
	v_addc_co_u32_e32 v1, vcc, 0, v1, vcc
	global_load_dwordx4 v[88:91], v[0:1], off
	global_load_dwordx4 v[98:101], v[0:1], off offset:512
	global_load_dwordx4 v[80:83], v[2:3], off offset:32
	global_load_dwordx4 v[84:87], v[2:3], off offset:64
	global_load_dwordx4 v[102:105], v[4:5], off offset:32
	global_load_dwordx4 v[92:95], v[2:3], off offset:96
	global_load_dwordx4 v[106:109], v[4:5], off offset:64
	global_load_dwordx4 v[110:113], v[4:5], off offset:96
	s_branch .LBB0_430

; __device__ __forceinline__ int crow(int r, int hi) { return (r & 3) + 8 * (r >> 2) + 4 * hi; }
; __device__ __forceinline__ unsigned cvtpk_s(float lo, float hi) { return pg8::cvt_pk_f16(lo, hi); }
; __device__ __forceinline__ int crow(int r, int hi) { return (r & 3) + 8 * (r >> 2) + 4 * hi; }
; template <bool MOBA, int THRL> ...
;     ...
;     { auto rr = __builtin_amdgcn_permlane32_swap(__float_as_uint(l_reg), __float_as_uint(l_reg), false, false); l_reg = __uint_as_float(rr[0]) + __uint_as_float(rr[1]); }
;     if (hi == 0) wsf[32 + r32] = l_reg; asm volatile("s_waitcnt lgkmcnt(0)" ::: "memory");
;     float rli[16];
; #pragma unroll
;     for (int r = 0; r < 16; ++r) rli[r] = __builtin_amdgcn_rcpf(wsf[32 + crow(r, hi)]);
;     {
;         int le = threadIdx.x & 63; asm volatile("" : "+v"(le));
;         float* stg = (float*)(shm + LDS_OST) + wid * 1024;
;         h16* Yw = Y + (rowbase + q0 + wid * QBLK) * 1536 + h * D;
; #pragma unroll
;         for (int d0 = 0; d0 < 2; ++d0) {
; #pragma unroll
;             for (int r = 0; r < 16; ++r) stg[crow(r, le >> 5) * 32 + (le & 31)] = o[d0][r] * rli[r];
;             asm volatile("s_waitcnt lgkmcnt(0)" ::: "memory");
; #pragma unroll
;             for (int i = 0; i < 2; ++i) { const int row = i * 16 + (le >> 2), ch = le & 3;
;                 const f32x4 a0 = *(const f32x4*)(stg + row * 32 + ch * 8), a1 = *(const f32x4*)(stg + row * 32 + ch * 8 + 4);
;                 const h16x8 zv = zpre[d0][i];
;                 float ov[8] = {a0[0], a0[1], a0[2], a0[3], a1[0], a1[1], a1[2], a1[3]};
; #pragma unroll
;                 for (int e = 0; e < 8; ++e) { const float zz = (float)zv[e]; ov[e] *= zz * __builtin_amdgcn_rcpf(1.f + __expf(-zz)); }
;                 u32x4 w; w.x = cvtpk_s(ov[0], ov[1]); w.y = cvtpk_s(ov[2], ov[3]); w.z = cvtpk_s(ov[4], ov[5]); w.w = cvtpk_s(ov[6], ov[7]);
;                 *(u32x4*)(Yw + (long)row * 1536 + d0 * 32 + ch * 8) = w; }
.LBB0_450:
	s_or_b64 exec, exec, s[0:1]
	s_waitcnt lgkmcnt(0)
	ds_read_b128 v[32:35], v227 offset:49280
	ds_read_b128 v[42:45], v227 offset:49312
	s_lshl_b32 s0, s89, 2
	s_add_i32 s11, s0, 0
	s_mul_i32 s0, s3, 0xc00
	s_waitcnt lgkmcnt(1)
	v_rcp_f32_e32 v38, v34
	v_rcp_f32_e32 v39, v35
	s_waitcnt lgkmcnt(0)
	v_rcp_f32_e32 v34, v44
	v_rcp_f32_e32 v35, v45
	ds_read_b128 v[44:47], v227 offset:49344
	ds_read_b128 v[48:51], v227 offset:49376
	v_rcp_f32_e32 v36, v42
	v_rcp_f32_e32 v40, v32
	v_rcp_f32_e32 v41, v33
	s_waitcnt lgkmcnt(1)
	v_rcp_f32_e32 v42, v46
	s_waitcnt lgkmcnt(0)
	v_rcp_f32_e32 v46, v50
	v_mov_b32_e32 v50, v250
	v_rcp_f32_e32 v37, v43
	v_and_b32_e32 v32, 31, v50
	v_rcp_f32_e32 v43, v47
	v_rcp_f32_e32 v47, v51
	v_lshlrev_b32_e32 v51, 2, v32
	v_ashrrev_i32_e32 v52, 2, v50
	v_lshlrev_b32_e32 v32, 3, v50
	v_lshlrev_b32_e32 v50, 4, v50
	v_and_b32_e32 v50, 0xfffffe00, v50
	v_add3_u32 v54, s11, v51, v50
	v_mul_f32_e32 v16, v16, v40
	v_mul_f32_e32 v17, v17, v41
	v_add_u32_e32 v50, 0xc800, v54
	ds_write2_b32 v50, v16, v17 offset1:32
	v_mul_f32_e32 v16, v18, v38
	v_mul_f32_e32 v17, v19, v39
	v_rcp_f32_e32 v45, v45
	ds_write2_b32 v50, v16, v17 offset0:64 offset1:96
	v_mul_f32_e32 v16, v20, v36
	s_waitcnt vmcnt(3)
	v_cvt_f32_f16_e32 v20, v76
	v_mul_f32_e32 v17, v21, v37
	v_add_u32_e32 v51, 0xcc00, v54
	v_rcp_f32_e32 v44, v44
	ds_write2_b32 v51, v16, v17 offset1:32
	v_mul_f32_e32 v16, v22, v34
	v_mul_f32_e32 v17, v23, v35
	ds_write2_b32 v51, v16, v17 offset0:64 offset1:96
	v_mul_f32_e32 v17, v25, v45
	v_mul_f32_e32 v25, 0xbfb8aa3b, v20
	v_rcp_f32_e32 v48, v48
	v_rcp_f32_e32 v49, v49
	v_exp_f32_e32 v25, v25
	v_cvt_f32_f16_sdwa v21, v76 dst_sel:DWORD dst_unused:UNUSED_PAD src0_sel:WORD_1
	v_mul_f32_e32 v16, v24, v44
	v_add_u32_e32 v22, 0xd000, v54
	ds_write2_b32 v22, v16, v17 offset1:32
	v_mul_f32_e32 v16, v26, v42
	v_mul_f32_e32 v17, v27, v43
	ds_write2_b32 v22, v16, v17 offset0:64 offset1:96
	v_mul_f32_e32 v16, v28, v48
	v_mul_f32_e32 v17, v29, v49
	v_add_u32_e32 v23, 0xd400, v54
	v_add_f32_e32 v25, 1.0, v25
	ds_write2_b32 v23, v16, v17 offset1:32
	v_mul_f32_e32 v16, v30, v46
	v_rcp_f32_e32 v30, v25
	v_mul_f32_e32 v25, 0xbfb8aa3b, v21
	v_exp_f32_e32 v25, v25
	v_and_b32_e32 v32, 24, v32
	v_mul_f32_e32 v17, v31, v47
	v_lshl_add_u32 v53, v32, 2, s11
	ds_write2_b32 v23, v16, v17 offset0:64 offset1:96
	v_add_f32_e32 v25, 1.0, v25
	s_waitcnt lgkmcnt(0)
	v_lshl_add_u32 v24, v52, 7, v53
	v_rcp_f32_e32 v31, v25
	ds_read_b128 v[26:29], v24 offset:51200
	ds_read_b128 v[16:19], v24 offset:51216
	s_mul_hi_u32 s1, s2, 0xc00
	s_add_i32 s1, s1, s0
	v_pk_mul_f32 v[20:21], v[30:31], v[20:21]
	s_mul_i32 s0, s2, 0xc00
	s_waitcnt lgkmcnt(1)
	v_pk_mul_f32 v[20:21], v[20:21], v[26:27]
	v_cvt_f32_f16_e32 v26, v77
	v_cvt_f32_f16_sdwa v27, v77 dst_sel:DWORD dst_unused:UNUSED_PAD src0_sel:WORD_1
	s_add_u32 s0, s60, s0
	s_addc_u32 s1, s61, s1
	v_mul_f32_e32 v25, 0xbfb8aa3b, v26
	v_exp_f32_e32 v25, v25
	v_lshlrev_b32_e32 v96, 1, v32
	v_lshl_add_u64 v[32:33], s[0:1], 0, v[96:97]
	v_add_u32_e32 v54, 16, v52
	v_add_f32_e32 v25, 1.0, v25
	v_rcp_f32_e32 v30, v25
	v_mul_f32_e32 v25, 0xbfb8aa3b, v27
	v_exp_f32_e32 v25, v25
	v_mul_f32_e32 v0, v0, v40
	v_mul_f32_e32 v1, v1, v41
	v_add_f32_e32 v25, 1.0, v25
	v_rcp_f32_e32 v31, v25
	s_nop 0
	v_pk_mul_f32 v[26:27], v[30:31], v[26:27]
	s_nop 0
	v_pk_mul_f32 v[26:27], v[26:27], v[28:29]
	v_cvt_f32_f16_e32 v28, v78
	v_cvt_f32_f16_sdwa v29, v78 dst_sel:DWORD dst_unused:UNUSED_PAD src0_sel:WORD_1
	v_mul_f32_e32 v25, 0xbfb8aa3b, v28
	v_exp_f32_e32 v25, v25
	s_nop 0
	v_add_f32_e32 v25, 1.0, v25
	v_rcp_f32_e32 v30, v25
	v_mul_f32_e32 v25, 0xbfb8aa3b, v29
	v_exp_f32_e32 v25, v25
	s_nop 0
	v_add_f32_e32 v25, 1.0, v25
	v_rcp_f32_e32 v31, v25
	s_nop 0
	v_pk_mul_f32 v[28:29], v[30:31], v[28:29]
	s_waitcnt lgkmcnt(0)
	v_pk_mul_f32 v[28:29], v[28:29], v[16:17]
	v_cvt_f32_f16_e32 v16, v79
	v_cvt_f32_f16_sdwa v17, v79 dst_sel:DWORD dst_unused:UNUSED_PAD src0_sel:WORD_1
	v_mul_f32_e32 v25, 0xbfb8aa3b, v16
	v_exp_f32_e32 v25, v25
	s_nop 0
	v_add_f32_e32 v25, 1.0, v25
	v_rcp_f32_e32 v30, v25
	v_mul_f32_e32 v25, 0xbfb8aa3b, v17
	v_exp_f32_e32 v25, v25
	s_nop 0
	v_add_f32_e32 v25, 1.0, v25
	v_rcp_f32_e32 v31, v25
	v_lshl_add_u32 v25, v54, 7, v53
	v_pk_mul_f32 v[16:17], v[30:31], v[16:17]
	s_nop 0
	v_pk_mul_f32 v[30:31], v[16:17], v[18:19]
	v_cvt_pk_f16_f32 v16, v20, v21
	v_cvt_pk_f16_f32 v19, v30, v31
	s_waitcnt vmcnt(1)
	v_cvt_f32_f16_sdwa v31, v72 dst_sel:DWORD dst_unused:UNUSED_PAD src0_sel:WORD_1
	v_cvt_f32_f16_e32 v30, v72
	v_mad_i64_i32 v[20:21], s[0:1], v52, s7, v[32:33]
	v_mul_f32_e32 v53, 0xbfb8aa3b, v31
	v_mul_f32_e32 v52, 0xbfb8aa3b, v30
	v_exp_f32_e32 v52, v52
	v_exp_f32_e32 v53, v53
	v_cvt_pk_f16_f32 v17, v26, v27
	v_cvt_pk_f16_f32 v18, v28, v29
	v_add_f32_e32 v52, 1.0, v52
	v_add_f32_e32 v53, 1.0, v53
	global_store_dwordx4 v[20:21], v[16:19], off sc1
	v_rcp_f32_e32 v52, v52
	v_rcp_f32_e32 v53, v53
	ds_read_b128 v[26:29], v25 offset:51200
	ds_read_b128 v[16:19], v25 offset:51216
	v_pk_mul_f32 v[30:31], v[52:53], v[30:31]
	s_waitcnt lgkmcnt(1)
	v_pk_mul_f32 v[26:27], v[30:31], v[26:27]
	v_cvt_f32_f16_sdwa v31, v73 dst_sel:DWORD dst_unused:UNUSED_PAD src0_sel:WORD_1
	v_cvt_f32_f16_e32 v30, v73
	v_cvt_pk_f16_f32 v26, v26, v27
	v_mul_f32_e32 v53, 0xbfb8aa3b, v31
	v_mul_f32_e32 v52, 0xbfb8aa3b, v30
	v_exp_f32_e32 v52, v52
	v_exp_f32_e32 v53, v53
	v_add_f32_e32 v52, 1.0, v52
	v_add_f32_e32 v53, 1.0, v53
	v_rcp_f32_e32 v52, v52
	v_rcp_f32_e32 v53, v53
	s_nop 0
	v_pk_mul_f32 v[30:31], v[52:53], v[30:31]
	s_nop 0
	v_pk_mul_f32 v[28:29], v[30:31], v[28:29]
	v_cvt_f32_f16_sdwa v31, v74 dst_sel:DWORD dst_unused:UNUSED_PAD src0_sel:WORD_1
	v_cvt_f32_f16_e32 v30, v74
	v_cvt_pk_f16_f32 v27, v28, v29
	v_mul_f32_e32 v53, 0xbfb8aa3b, v31
	v_mul_f32_e32 v52, 0xbfb8aa3b, v30
	v_exp_f32_e32 v52, v52
	v_exp_f32_e32 v53, v53
	v_add_f32_e32 v52, 1.0, v52
	v_add_f32_e32 v53, 1.0, v53
	v_rcp_f32_e32 v52, v52
	v_rcp_f32_e32 v53, v53
	s_nop 0
	v_pk_mul_f32 v[30:31], v[52:53], v[30:31]
	s_waitcnt lgkmcnt(0)
; __device__ __forceinline__ int crow(int r, int hi) { return (r & 3) + 8 * (r >> 2) + 4 * hi; }
; __device__ __forceinline__ unsigned cvtpk_s(float lo, float hi) { return pg8::cvt_pk_f16(lo, hi); }
; __device__ __forceinline__ int crow(int r, int hi) { return (r & 3) + 8 * (r >> 2) + 4 * hi; }
; template <bool MOBA, int THRL> ...
;     ...
;             for (int r = 0; r < 16; ++r) stg[crow(r, le >> 5) * 32 + (le & 31)] = o[d0][r] * rli[r];
;             asm volatile("s_waitcnt lgkmcnt(0)" ::: "memory");
; #pragma unroll
;             for (int i = 0; i < 2; ++i) { const int row = i * 16 + (le >> 2), ch = le & 3;
;                 const f32x4 a0 = *(const f32x4*)(stg + row * 32 + ch * 8), a1 = *(const f32x4*)(stg + row * 32 + ch * 8 + 4);
;                 const h16x8 zv = zpre[d0][i];
;                 float ov[8] = {a0[0], a0[1], a0[2], a0[3], a1[0], a1[1], a1[2], a1[3]};
; #pragma unroll
;                 for (int e = 0; e < 8; ++e) { const float zz = (float)zv[e]; ov[e] *= zz * __builtin_amdgcn_rcpf(1.f + __expf(-zz)); }
;                 u32x4 w; w.x = cvtpk_s(ov[0], ov[1]); w.y = cvtpk_s(ov[2], ov[3]); w.z = cvtpk_s(ov[4], ov[5]); w.w = cvtpk_s(ov[6], ov[7]);
;                 *(u32x4*)(Yw + (long)row * 1536 + d0 * 32 + ch * 8) = w; }
;             asm volatile("s_waitcnt lgkmcnt(0)" ::: "memory");
;         }
;     }
;     asm volatile("s_waitcnt lgkmcnt(0)\n\ts_barrier" ::: "memory");
; __global__ void __launch_bounds__(NTHREADS, 2) mega(MArgs a) {
;     ...
;                 for (int i = 0; i < 4; ++i) {
	v_pk_mul_f32 v[16:17], v[30:31], v[16:17]
	v_cvt_f32_f16_sdwa v31, v75 dst_sel:DWORD dst_unused:UNUSED_PAD src0_sel:WORD_1
	v_cvt_f32_f16_e32 v30, v75
	v_cvt_pk_f16_f32 v28, v16, v17
	v_mad_i64_i32 v[16:17], s[0:1], v54, s7, v[32:33]
	v_mul_f32_e32 v52, 0xbfb8aa3b, v30
	v_mul_f32_e32 v53, 0xbfb8aa3b, v31
	v_exp_f32_e32 v52, v52
	v_exp_f32_e32 v53, v53
	v_add_f32_e32 v52, 1.0, v52
	v_add_f32_e32 v53, 1.0, v53
	v_rcp_f32_e32 v52, v52
	v_rcp_f32_e32 v53, v53
	s_nop 0
	v_pk_mul_f32 v[30:31], v[52:53], v[30:31]
	s_nop 0
	v_pk_mul_f32 v[18:19], v[30:31], v[18:19]
	s_nop 0
	v_cvt_pk_f16_f32 v29, v18, v19
	global_store_dwordx4 v[16:17], v[26:29], off sc1
	s_waitcnt lgkmcnt(0)
	ds_write2_b32 v50, v0, v1 offset1:32
	v_mul_f32_e32 v0, v2, v38
	v_mul_f32_e32 v1, v3, v39
	ds_write2_b32 v50, v0, v1 offset0:64 offset1:96
	v_mul_f32_e32 v0, v4, v36
	v_mul_f32_e32 v1, v5, v37
	ds_write2_b32 v51, v0, v1 offset1:32
	v_mul_f32_e32 v0, v6, v34
	v_mul_f32_e32 v1, v7, v35
	ds_write2_b32 v51, v0, v1 offset0:64 offset1:96
	v_mul_f32_e32 v0, v8, v44
	v_mul_f32_e32 v1, v9, v45
	v_cvt_f32_f16_sdwa v9, v68 dst_sel:DWORD dst_unused:UNUSED_PAD src0_sel:WORD_1
	v_cvt_f32_f16_e32 v8, v68
	ds_write2_b32 v22, v0, v1 offset1:32
	v_mul_f32_e32 v0, v10, v42
	v_mul_f32_e32 v1, v11, v43
	v_mul_f32_e32 v10, 0xbfb8aa3b, v8
	v_mul_f32_e32 v11, 0xbfb8aa3b, v9
	v_exp_f32_e32 v10, v10
	v_exp_f32_e32 v11, v11
	ds_write2_b32 v22, v0, v1 offset0:64 offset1:96
	v_mul_f32_e32 v0, v12, v48
	v_mul_f32_e32 v1, v13, v49
	ds_write2_b32 v23, v0, v1 offset1:32
	v_mul_f32_e32 v0, v14, v46
	v_mul_f32_e32 v1, v15, v47
	ds_write2_b32 v23, v0, v1 offset0:64 offset1:96
	v_add_f32_e32 v10, 1.0, v10
	v_add_f32_e32 v11, 1.0, v11
	s_waitcnt lgkmcnt(0)
	v_rcp_f32_e32 v10, v10
	v_rcp_f32_e32 v11, v11
	ds_read_b128 v[4:7], v24 offset:51200
	ds_read_b128 v[0:3], v24 offset:51216
	v_pk_mul_f32 v[8:9], v[10:11], v[8:9]
	s_waitcnt lgkmcnt(1)
	v_pk_mul_f32 v[4:5], v[8:9], v[4:5]
	v_cvt_f32_f16_sdwa v9, v69 dst_sel:DWORD dst_unused:UNUSED_PAD src0_sel:WORD_1
	v_cvt_f32_f16_e32 v8, v69
	v_mul_f32_e32 v11, 0xbfb8aa3b, v9
	v_mul_f32_e32 v10, 0xbfb8aa3b, v8
	v_exp_f32_e32 v10, v10
	v_exp_f32_e32 v11, v11
	v_add_f32_e32 v10, 1.0, v10
	v_add_f32_e32 v11, 1.0, v11
	v_rcp_f32_e32 v10, v10
	v_rcp_f32_e32 v11, v11
	s_nop 0
	v_pk_mul_f32 v[8:9], v[10:11], v[8:9]
	s_nop 0
	v_pk_mul_f32 v[6:7], v[8:9], v[6:7]
	v_cvt_f32_f16_sdwa v9, v70 dst_sel:DWORD dst_unused:UNUSED_PAD src0_sel:WORD_1
	v_cvt_f32_f16_e32 v8, v70
	v_mul_f32_e32 v11, 0xbfb8aa3b, v9
	v_mul_f32_e32 v10, 0xbfb8aa3b, v8
	v_exp_f32_e32 v10, v10
	v_exp_f32_e32 v11, v11
	v_add_f32_e32 v10, 1.0, v10
	v_add_f32_e32 v11, 1.0, v11
	v_rcp_f32_e32 v10, v10
	v_rcp_f32_e32 v11, v11
	s_nop 0
	v_pk_mul_f32 v[8:9], v[10:11], v[8:9]
	s_waitcnt lgkmcnt(0)
	v_pk_mul_f32 v[8:9], v[8:9], v[0:1]
	v_cvt_f32_f16_sdwa v1, v71 dst_sel:DWORD dst_unused:UNUSED_PAD src0_sel:WORD_1
	v_cvt_f32_f16_e32 v0, v71
	v_mul_f32_e32 v11, 0xbfb8aa3b, v1
	v_mul_f32_e32 v10, 0xbfb8aa3b, v0
	v_exp_f32_e32 v10, v10
	v_exp_f32_e32 v11, v11
	v_add_f32_e32 v10, 1.0, v10
	v_add_f32_e32 v11, 1.0, v11
	v_rcp_f32_e32 v10, v10
	v_rcp_f32_e32 v11, v11
	s_nop 0
	v_pk_mul_f32 v[0:1], v[10:11], v[0:1]
	s_nop 0
	v_pk_mul_f32 v[10:11], v[0:1], v[2:3]
	v_cvt_pk_f16_f32 v2, v8, v9
	s_waitcnt vmcnt(2)
	v_cvt_f32_f16_sdwa v9, v64 dst_sel:DWORD dst_unused:UNUSED_PAD src0_sel:WORD_1
	v_cvt_f32_f16_e32 v8, v64
	v_cvt_pk_f16_f32 v3, v10, v11
	v_cvt_pk_f16_f32 v0, v4, v5
	v_mul_f32_e32 v11, 0xbfb8aa3b, v9
	v_mul_f32_e32 v10, 0xbfb8aa3b, v8
	v_exp_f32_e32 v10, v10
	v_exp_f32_e32 v11, v11
	v_cvt_pk_f16_f32 v1, v6, v7
	global_store_dwordx4 v[20:21], v[0:3], off offset:64 sc1
	v_add_f32_e32 v10, 1.0, v10
	v_add_f32_e32 v11, 1.0, v11
	v_rcp_f32_e32 v10, v10
	v_rcp_f32_e32 v11, v11
	ds_read_b128 v[4:7], v25 offset:51200
	ds_read_b128 v[0:3], v25 offset:51216
	v_pk_mul_f32 v[8:9], v[10:11], v[8:9]
	s_waitcnt lgkmcnt(1)
	v_pk_mul_f32 v[4:5], v[8:9], v[4:5]
	v_cvt_f32_f16_sdwa v9, v65 dst_sel:DWORD dst_unused:UNUSED_PAD src0_sel:WORD_1
	v_cvt_f32_f16_e32 v8, v65
	v_mul_f32_e32 v11, 0xbfb8aa3b, v9
	v_mul_f32_e32 v10, 0xbfb8aa3b, v8
	v_exp_f32_e32 v10, v10
	v_exp_f32_e32 v11, v11
	v_add_f32_e32 v10, 1.0, v10
	v_add_f32_e32 v11, 1.0, v11
	v_rcp_f32_e32 v10, v10
	v_rcp_f32_e32 v11, v11
	s_nop 0
	v_pk_mul_f32 v[8:9], v[10:11], v[8:9]
	s_nop 0
	v_pk_mul_f32 v[6:7], v[8:9], v[6:7]
	v_cvt_f32_f16_sdwa v9, v66 dst_sel:DWORD dst_unused:UNUSED_PAD src0_sel:WORD_1
	v_cvt_f32_f16_e32 v8, v66
	v_mul_f32_e32 v11, 0xbfb8aa3b, v9
	v_mul_f32_e32 v10, 0xbfb8aa3b, v8
	v_exp_f32_e32 v10, v10
	v_exp_f32_e32 v11, v11
	v_add_f32_e32 v10, 1.0, v10
	v_add_f32_e32 v11, 1.0, v11
	v_rcp_f32_e32 v10, v10
	v_rcp_f32_e32 v11, v11
	s_nop 0
	v_pk_mul_f32 v[8:9], v[10:11], v[8:9]
	s_waitcnt lgkmcnt(0)
	v_pk_mul_f32 v[8:9], v[8:9], v[0:1]
	v_cvt_f32_f16_sdwa v1, v67 dst_sel:DWORD dst_unused:UNUSED_PAD src0_sel:WORD_1
	v_cvt_f32_f16_e32 v0, v67
	v_mul_f32_e32 v11, 0xbfb8aa3b, v1
	v_mul_f32_e32 v10, 0xbfb8aa3b, v0
	v_exp_f32_e32 v10, v10
	v_exp_f32_e32 v11, v11
	v_add_f32_e32 v10, 1.0, v10
	v_add_f32_e32 v11, 1.0, v11
	v_rcp_f32_e32 v10, v10
	v_rcp_f32_e32 v11, v11
	s_nop 0
	v_pk_mul_f32 v[0:1], v[10:11], v[0:1]
	s_nop 0
	v_pk_mul_f32 v[10:11], v[0:1], v[2:3]
	v_cvt_pk_f16_f32 v0, v4, v5
	v_cvt_pk_f16_f32 v1, v6, v7
	v_cvt_pk_f16_f32 v2, v8, v9
	v_cvt_pk_f16_f32 v3, v10, v11
	global_store_dwordx4 v[16:17], v[0:3], off offset:64 sc1
	s_waitcnt lgkmcnt(0)
	s_waitcnt lgkmcnt(0)
	s_barrier
	s_add_i32 s12, s12, 1
	s_cmp_eq_u32 s12, 4
	s_cbranch_scc1 .LBB0_448

; #define SBAR() __builtin_amdgcn_sched_barrier(0)
; #define PKW(P, B) cvtpk_s(P[B], P[B + 1])
; __device__ __forceinline__ void pv(f32x16* o, int vb, s16x8 pa0, s16x8 pa1, s16x8 pa2, s16x8 pa3) {
; #pragma unroll
;     for (int d0 = 0; d0 < 2; ++d0) { s16x4 lo[4], hi[4];
; #pragma unroll
;         for (int ks = 0; ks < 4; ++ks) {
;             asm volatile("ds_read_b64_tr_b16 %0,%1 offset:%c2" : "=&v"(lo[ks]) : "v"(vb), "i"(d0 * 4096 + ks * 1024) : "memory");
;             asm volatile("ds_read_b64_tr_b16 %0,%1 offset:%c2" : "=&v"(hi[ks]) : "v"(vb), "i"(d0 * 4096 + ks * 1024 + 512) : "memory"); }
;         asm volatile("s_waitcnt lgkmcnt(0)" ::: "memory"); SBAR();
;     ...
;         o[d0] = MFMA32(pa0, PK(0), o[d0]);
;         o[d0] = MFMA32(pa1, PK(1), o[d0]);
;         o[d0] = MFMA32(pa2, PK(2), o[d0]);
;         o[d0] = MFMA32(pa3, PK(3), o[d0]);
;     ...
;     }
; }
; template <bool MOBA, int THRL> ...
;     ...
;     h16x8 zpre[2][2];
;     {   int lz = threadIdx.x & 63; asm volatile("" : "+v"(lz));
;         const h16* zp = Z + (rowbase + q0 + wid * QBLK + (lz >> 2)) * PQ + h * D + (lz & 3) * 8;
; #pragma unroll
;         for (int d0 = 0; d0 < 2; ++d0)
; #pragma unroll
;             for (int i = 0; i < 2; ++i) zpre[d0][i] = *(const h16x8*)(zp + (long)(i * 16) * PQ + d0 * 32); }
;     { float sacc = pB0[0] + pB0[1]; _Pragma("unroll") for (int r = 2; r < 16; ++r) sacc += pB0[r]; _Pragma("unroll") for (int r = 0; r < 16; ++r) sacc += pB1[r]; l_reg += sacc;
;       pw0 = (u32x4){PKW(pB0, 0), PKW(pB0, 2), PKW(pB0, 4), PKW(pB0, 6)}; pw1 = (u32x4){PKW(pB0, 8), PKW(pB0, 10), PKW(pB0, 12), PKW(pB0, 14)}; pw2 = (u32x4){PKW(pB1, 0), PKW(pB1, 2), PKW(pB1, 4), PKW(pB1, 6)}; pw3 = (u32x4){PKW(pB1, 8), PKW(pB1, 10), PKW(pB1, 12), PKW(pB1, 14)};
;       int ln_ = threadIdx.x & 63; asm volatile("" : "+v"(ln_));
;       const int vb0 = (int)(lds0 + LDS_V) + ((ln_ >> 4) & 1) * 32 + (ln_ & 3) * 8 + (4 * (ln_ >> 5) + ((ln_ & 15) >> 2)) * 64;
;       SBAR(); pv(o, vb0 + sl_cur, PAF(0), PAF(1), PAF(2), PAF(3)); }
;     ...
;     { auto rr = __builtin_amdgcn_permlane32_swap(__float_as_uint(l_reg), __float_as_uint(l_reg), false, false); l_reg = __uint_as_float(rr[0]) + __uint_as_float(rr[1]); }
;     if (hi == 0) wsf[32 + r32] = l_reg; asm volatile("s_waitcnt lgkmcnt(0)" ::: "memory");
;     float rli[16];
; #pragma unroll
;     for (int r = 0; r < 16; ++r) rli[r] = __builtin_amdgcn_rcpf(wsf[32 + crow(r, hi)]);
.LBB0_580:
	v_mov_b32_e32 v84, v250
	v_mov_b64_e32 v[82:83], s[52:53]
	v_ashrrev_i32_e32 v80, 2, v84
	v_ashrrev_i32_e32 v81, 31, v80
	v_lshl_add_u64 v[80:81], s[66:67], 0, v[80:81]
	v_mad_u64_u32 v[82:83], s[0:1], v80, s91, v[82:83]
	v_mov_b32_e32 v80, v83
	v_mad_u64_u32 v[80:81], s[0:1], v81, s91, v[80:81]
	v_mov_b32_e32 v83, v80
	v_lshlrev_b32_e32 v80, 4, v84
	v_and_b32_e32 v96, 48, v80
	v_lshl_add_u64 v[80:81], v[82:83], 0, v[96:97]
	s_mov_b32 s96, 0x38000
	v_add_co_u32_e32 v82, vcc, s96, v80
	v_add_f32_e32 v96, v48, v49
	s_nop 0
	v_addc_co_u32_e32 v83, vcc, 0, v81, vcc
	global_load_dwordx4 v[92:95], v[80:81], off
	global_load_dwordx4 v[84:87], v[80:81], off offset:64
	global_load_dwordx4 v[88:91], v[82:83], off
	s_nop 0
	global_load_dwordx4 v[80:83], v[82:83], off offset:64
	v_add_f32_e32 v96, v50, v96
	v_add_f32_e32 v96, v51, v96
	v_add_f32_e32 v96, v52, v96
	v_add_f32_e32 v96, v53, v96
	v_add_f32_e32 v96, v54, v96
	v_add_f32_e32 v96, v55, v96
	v_add_f32_e32 v96, v56, v96
	v_add_f32_e32 v96, v57, v96
	v_add_f32_e32 v96, v58, v96
	v_add_f32_e32 v96, v59, v96
	v_add_f32_e32 v96, v60, v96
	v_add_f32_e32 v96, v61, v96
	v_add_f32_e32 v96, v62, v96
	v_add_f32_e32 v96, v63, v96
	v_add_f32_e32 v96, v32, v96
	v_add_f32_e32 v96, v33, v96
	v_add_f32_e32 v96, v34, v96
	v_add_f32_e32 v96, v35, v96
	v_add_f32_e32 v96, v36, v96
	v_add_f32_e32 v96, v37, v96
	v_add_f32_e32 v96, v38, v96
	v_add_f32_e32 v96, v39, v96
	v_add_f32_e32 v96, v40, v96
	v_add_f32_e32 v96, v41, v96
	v_add_f32_e32 v96, v42, v96
	v_add_f32_e32 v96, v43, v96
	v_add_f32_e32 v96, v44, v96
	v_add_f32_e32 v96, v45, v96
	v_cvt_pk_f16_f32 v32, v32, v33
	v_cvt_pk_f16_f32 v33, v34, v35
	v_cvt_pk_f16_f32 v34, v36, v37
	v_cvt_pk_f16_f32 v36, v40, v41
	v_mov_b32_e32 v40, v250
	v_add_f32_e32 v96, v46, v96
	v_add_f32_e32 v96, v47, v96
	v_cvt_pk_f16_f32 v37, v42, v43
	v_lshlrev_b32_e32 v41, 1, v40
	v_lshlrev_b32_e32 v42, 3, v40
	v_lshrrev_b32_e32 v43, 3, v40
	v_bfe_u32 v40, v40, 2, 2
	s_mov_b32 s97, 0x3fffffc
	v_add_f32_e32 v96, v120, v96
	v_and_or_b32 v40, v43, s97, v40
	v_cvt_pk_f16_f32 v48, v48, v49
	v_cvt_pk_f16_f32 v49, v50, v51
	v_cvt_pk_f16_f32 v50, v52, v53
	v_cvt_pk_f16_f32 v51, v54, v55
	v_cvt_pk_f16_f32 v52, v56, v57
	v_cvt_pk_f16_f32 v53, v58, v59
	v_cvt_pk_f16_f32 v54, v60, v61
	v_cvt_pk_f16_f32 v55, v62, v63
	v_cvt_pk_f16_f32 v35, v38, v39
	v_cvt_pk_f16_f32 v38, v44, v45
	v_cvt_pk_f16_f32 v39, v46, v47
	v_and_b32_e32 v41, 32, v41
	v_and_b32_e32 v42, 24, v42
	v_lshlrev_b32_e32 v40, 6, v40
	s_cmp_lg_u32 0, -1
	s_cselect_b32 s0, 0, 0
	s_add_i32 s0, s0, s45
	s_addk_i32 s0, 0x6000
	v_add_u32_e32 v41, s0, v41
	v_add3_u32 v98, v41, v42, v40
	ds_read_b64_tr_b16 v[40:41],v98 offset:0
	ds_read_b64_tr_b16 v[42:43],v98 offset:512
	ds_read_b64_tr_b16 v[44:45],v98 offset:1024
	ds_read_b64_tr_b16 v[46:47],v98 offset:1536
	ds_read_b64_tr_b16 v[56:57],v98 offset:2048
	ds_read_b64_tr_b16 v[58:59],v98 offset:2560
	ds_read_b64_tr_b16 v[60:61],v98 offset:3072
	ds_read_b64_tr_b16 v[62:63],v98 offset:3584
	s_waitcnt lgkmcnt(0)
	s_nop 0
	v_mfma_f32_32x32x16_f16 v[16:31], v[48:51], v[40:43], v[16:31]
	ds_read_b64_tr_b16 v[40:41],v98 offset:4096
	ds_read_b64_tr_b16 v[42:43],v98 offset:4608
	v_mfma_f32_32x32x16_f16 v[16:31], v[52:55], v[44:47], v[16:31]
	ds_read_b64_tr_b16 v[44:45],v98 offset:5120
	ds_read_b64_tr_b16 v[46:47],v98 offset:5632
	v_mfma_f32_32x32x16_f16 v[16:31], v[32:35], v[56:59], v[16:31]
	ds_read_b64_tr_b16 v[56:57],v98 offset:6144
	ds_read_b64_tr_b16 v[58:59],v98 offset:6656
	v_mfma_f32_32x32x16_f16 v[16:31], v[36:39], v[60:63], v[16:31]
	ds_read_b64_tr_b16 v[60:61],v98 offset:7168
	ds_read_b64_tr_b16 v[62:63],v98 offset:7680
	s_waitcnt lgkmcnt(0)
	v_mfma_f32_32x32x16_f16 v[0:15], v[48:51], v[40:43], v[0:15]
	v_cmp_gt_u32_e32 vcc, 32, v226
	v_mfma_f32_32x32x16_f16 v[0:15], v[52:55], v[44:47], v[0:15]
	v_mfma_f32_32x32x16_f16 v[0:15], v[32:35], v[56:59], v[0:15]
	v_mov_b32_e32 v32, v96
	s_nop 1
	v_permlane32_swap_b32_e32 v96, v32
	v_mfma_f32_32x32x16_f16 v[0:15], v[36:39], v[60:63], v[0:15]
	s_and_saveexec_b64 s[0:1], vcc
	v_add_f32_e32 v32, v96, v32
	ds_write_b32 v229, v32 offset:49280
	s_or_b64 exec, exec, s[0:1]
	s_waitcnt lgkmcnt(0)
	ds_read_b128 v[32:35], v228 offset:49280
	ds_read_b128 v[42:45], v228 offset:49312
	s_lshl_b32 s0, s90, 2
	s_add_i32 s2, s0, 0
	s_mul_i32 s0, s67, 0xc00
	s_waitcnt lgkmcnt(1)
	v_rcp_f32_e32 v38, v34
	v_rcp_f32_e32 v39, v35
	s_waitcnt lgkmcnt(0)
	v_rcp_f32_e32 v34, v44
	v_rcp_f32_e32 v35, v45
	ds_read_b128 v[44:47], v228 offset:49344
	ds_read_b128 v[48:51], v228 offset:49376
	v_rcp_f32_e32 v36, v42
	v_rcp_f32_e32 v40, v32
	v_rcp_f32_e32 v41, v33
	s_waitcnt lgkmcnt(1)
	v_rcp_f32_e32 v42, v46
	s_waitcnt lgkmcnt(0)
	v_rcp_f32_e32 v46, v50
	v_mov_b32_e32 v50, v250
	v_rcp_f32_e32 v37, v43
	v_and_b32_e32 v32, 31, v50
	v_rcp_f32_e32 v43, v47
	v_rcp_f32_e32 v47, v51
	v_lshlrev_b32_e32 v51, 2, v32
	v_ashrrev_i32_e32 v52, 2, v50
	v_lshlrev_b32_e32 v32, 3, v50
	v_lshlrev_b32_e32 v50, 4, v50
	v_and_b32_e32 v50, 0xfffffe00, v50
	v_add3_u32 v54, s2, v51, v50
	v_mul_f32_e32 v16, v16, v40
	v_mul_f32_e32 v17, v17, v41
	v_add_u32_e32 v50, 0xc800, v54
	ds_write2_b32 v50, v16, v17 offset1:32
	v_mul_f32_e32 v16, v18, v38
	v_mul_f32_e32 v17, v19, v39
	v_rcp_f32_e32 v45, v45
	ds_write2_b32 v50, v16, v17 offset0:64 offset1:96
	v_mul_f32_e32 v16, v20, v36
	s_waitcnt vmcnt(3)
; __device__ __forceinline__ int crow(int r, int hi) { return (r & 3) + 8 * (r >> 2) + 4 * hi; }
; __device__ __forceinline__ unsigned cvtpk_s(float lo, float hi) { return pg8::cvt_pk_f16(lo, hi); }
; __device__ __forceinline__ int crow(int r, int hi) { return (r & 3) + 8 * (r >> 2) + 4 * hi; }
; template <bool MOBA, int THRL> ...
;     ...
;         for (int d0 = 0; d0 < 2; ++d0) {
; #pragma unroll
;             for (int r = 0; r < 16; ++r) stg[crow(r, le >> 5) * 32 + (le & 31)] = o[d0][r] * rli[r];
;             asm volatile("s_waitcnt lgkmcnt(0)" ::: "memory");
; #pragma unroll
;             for (int i = 0; i < 2; ++i) { const int row = i * 16 + (le >> 2), ch = le & 3;
;                 const f32x4 a0 = *(const f32x4*)(stg + row * 32 + ch * 8), a1 = *(const f32x4*)(stg + row * 32 + ch * 8 + 4);
;                 const h16x8 zv = zpre[d0][i];
;                 float ov[8] = {a0[0], a0[1], a0[2], a0[3], a1[0], a1[1], a1[2], a1[3]};
; #pragma unroll
;                 for (int e = 0; e < 8; ++e) { const float zz = (float)zv[e]; ov[e] *= zz * __builtin_amdgcn_rcpf(1.f + __expf(-zz)); }
;                 u32x4 w; w.x = cvtpk_s(ov[0], ov[1]); w.y = cvtpk_s(ov[2], ov[3]); w.z = cvtpk_s(ov[4], ov[5]); w.w = cvtpk_s(ov[6], ov[7]);
;                 *(u32x4*)(Yw + (long)row * 1536 + d0 * 32 + ch * 8) = w; }
	v_cvt_f32_f16_e32 v20, v92
	v_mul_f32_e32 v17, v21, v37
	v_add_u32_e32 v51, 0xcc00, v54
	v_rcp_f32_e32 v44, v44
	ds_write2_b32 v51, v16, v17 offset1:32
	v_mul_f32_e32 v16, v22, v34
	v_mul_f32_e32 v17, v23, v35
	ds_write2_b32 v51, v16, v17 offset0:64 offset1:96
	v_mul_f32_e32 v17, v25, v45
	v_mul_f32_e32 v25, 0xbfb8aa3b, v20
	v_rcp_f32_e32 v48, v48
	v_rcp_f32_e32 v49, v49
	v_exp_f32_e32 v25, v25
	v_cvt_f32_f16_sdwa v21, v92 dst_sel:DWORD dst_unused:UNUSED_PAD src0_sel:WORD_1
	v_mul_f32_e32 v16, v24, v44
	v_add_u32_e32 v22, 0xd000, v54
	ds_write2_b32 v22, v16, v17 offset1:32
	v_mul_f32_e32 v16, v26, v42
	v_mul_f32_e32 v17, v27, v43
	ds_write2_b32 v22, v16, v17 offset0:64 offset1:96
	v_mul_f32_e32 v16, v28, v48
	v_mul_f32_e32 v17, v29, v49
	v_add_u32_e32 v23, 0xd400, v54
	v_add_f32_e32 v25, 1.0, v25
	ds_write2_b32 v23, v16, v17 offset1:32
	v_mul_f32_e32 v16, v30, v46
	v_rcp_f32_e32 v30, v25
	v_mul_f32_e32 v25, 0xbfb8aa3b, v21
	v_exp_f32_e32 v25, v25
	v_and_b32_e32 v32, 24, v32
	v_mul_f32_e32 v17, v31, v47
	v_lshl_add_u32 v53, v32, 2, s2
	ds_write2_b32 v23, v16, v17 offset0:64 offset1:96
	v_add_f32_e32 v25, 1.0, v25
	s_waitcnt lgkmcnt(0)
	v_lshl_add_u32 v24, v52, 7, v53
	v_rcp_f32_e32 v31, v25
	ds_read_b128 v[26:29], v24 offset:51200
	ds_read_b128 v[16:19], v24 offset:51216
	s_mul_hi_u32 s1, s66, 0xc00
	s_add_i32 s1, s1, s0
	v_pk_mul_f32 v[20:21], v[30:31], v[20:21]
	s_mul_i32 s0, s66, 0xc00
	s_waitcnt lgkmcnt(1)
	v_pk_mul_f32 v[20:21], v[20:21], v[26:27]
	v_cvt_f32_f16_e32 v26, v93
	v_cvt_f32_f16_sdwa v27, v93 dst_sel:DWORD dst_unused:UNUSED_PAD src0_sel:WORD_1
	s_add_u32 s0, s27, s0
	s_addc_u32 s1, s6, s1
	v_mul_f32_e32 v25, 0xbfb8aa3b, v26
	v_exp_f32_e32 v25, v25
	v_lshlrev_b32_e32 v96, 1, v32
	v_lshl_add_u64 v[32:33], s[0:1], 0, v[96:97]
	v_add_u32_e32 v54, 16, v52
	v_add_f32_e32 v25, 1.0, v25
	v_rcp_f32_e32 v30, v25
	v_mul_f32_e32 v25, 0xbfb8aa3b, v27
	v_exp_f32_e32 v25, v25
	v_mul_f32_e32 v0, v0, v40
	v_mul_f32_e32 v1, v1, v41
	v_add_f32_e32 v25, 1.0, v25
	v_rcp_f32_e32 v31, v25
	s_nop 0
	v_pk_mul_f32 v[26:27], v[30:31], v[26:27]
	s_nop 0
	v_pk_mul_f32 v[26:27], v[26:27], v[28:29]
	v_cvt_f32_f16_e32 v28, v94
	v_cvt_f32_f16_sdwa v29, v94 dst_sel:DWORD dst_unused:UNUSED_PAD src0_sel:WORD_1
	v_mul_f32_e32 v25, 0xbfb8aa3b, v28
	v_exp_f32_e32 v25, v25
	s_nop 0
	v_add_f32_e32 v25, 1.0, v25
	v_rcp_f32_e32 v30, v25
	v_mul_f32_e32 v25, 0xbfb8aa3b, v29
	v_exp_f32_e32 v25, v25
	s_nop 0
	v_add_f32_e32 v25, 1.0, v25
	v_rcp_f32_e32 v31, v25
	s_nop 0
	v_pk_mul_f32 v[28:29], v[30:31], v[28:29]
	s_waitcnt lgkmcnt(0)
	v_pk_mul_f32 v[28:29], v[28:29], v[16:17]
	v_cvt_f32_f16_e32 v16, v95
	v_cvt_f32_f16_sdwa v17, v95 dst_sel:DWORD dst_unused:UNUSED_PAD src0_sel:WORD_1
	v_mul_f32_e32 v25, 0xbfb8aa3b, v16
	v_exp_f32_e32 v25, v25
	s_nop 0
	v_add_f32_e32 v25, 1.0, v25
	v_rcp_f32_e32 v30, v25
	v_mul_f32_e32 v25, 0xbfb8aa3b, v17
	v_exp_f32_e32 v25, v25
	s_nop 0
	v_add_f32_e32 v25, 1.0, v25
	v_rcp_f32_e32 v31, v25
	v_lshl_add_u32 v25, v54, 7, v53
	v_pk_mul_f32 v[16:17], v[30:31], v[16:17]
	s_nop 0
	v_pk_mul_f32 v[30:31], v[16:17], v[18:19]
	v_cvt_pk_f16_f32 v16, v20, v21
	v_cvt_pk_f16_f32 v19, v30, v31
	s_waitcnt vmcnt(1)
	v_cvt_f32_f16_sdwa v31, v88 dst_sel:DWORD dst_unused:UNUSED_PAD src0_sel:WORD_1
	v_cvt_f32_f16_e32 v30, v88
	v_mad_i64_i32 v[20:21], s[0:1], v52, s7, v[32:33]
	v_mul_f32_e32 v53, 0xbfb8aa3b, v31
	v_mul_f32_e32 v52, 0xbfb8aa3b, v30
	v_exp_f32_e32 v52, v52
	v_exp_f32_e32 v53, v53
	v_cvt_pk_f16_f32 v17, v26, v27
	v_cvt_pk_f16_f32 v18, v28, v29
	v_add_f32_e32 v52, 1.0, v52
	v_add_f32_e32 v53, 1.0, v53
	global_store_dwordx4 v[20:21], v[16:19], off sc1
	v_rcp_f32_e32 v52, v52
	v_rcp_f32_e32 v53, v53
	ds_read_b128 v[26:29], v25 offset:51200
	ds_read_b128 v[16:19], v25 offset:51216
	v_pk_mul_f32 v[30:31], v[52:53], v[30:31]
	s_waitcnt lgkmcnt(1)
	v_pk_mul_f32 v[26:27], v[30:31], v[26:27]
	v_cvt_f32_f16_sdwa v31, v89 dst_sel:DWORD dst_unused:UNUSED_PAD src0_sel:WORD_1
	v_cvt_f32_f16_e32 v30, v89
	v_cvt_pk_f16_f32 v26, v26, v27
	v_mul_f32_e32 v53, 0xbfb8aa3b, v31
	v_mul_f32_e32 v52, 0xbfb8aa3b, v30
	v_exp_f32_e32 v52, v52
	v_exp_f32_e32 v53, v53
	v_add_f32_e32 v52, 1.0, v52
	v_add_f32_e32 v53, 1.0, v53
	v_rcp_f32_e32 v52, v52
	v_rcp_f32_e32 v53, v53
	s_nop 0
	v_pk_mul_f32 v[30:31], v[52:53], v[30:31]
	s_nop 0
	v_pk_mul_f32 v[28:29], v[30:31], v[28:29]
	v_cvt_f32_f16_sdwa v31, v90 dst_sel:DWORD dst_unused:UNUSED_PAD src0_sel:WORD_1
	v_cvt_f32_f16_e32 v30, v90
	v_cvt_pk_f16_f32 v27, v28, v29
	v_mul_f32_e32 v53, 0xbfb8aa3b, v31
	v_mul_f32_e32 v52, 0xbfb8aa3b, v30
	v_exp_f32_e32 v52, v52
	v_exp_f32_e32 v53, v53
	v_add_f32_e32 v52, 1.0, v52
	v_add_f32_e32 v53, 1.0, v53
	v_rcp_f32_e32 v52, v52
	v_rcp_f32_e32 v53, v53
	s_nop 0
	v_pk_mul_f32 v[30:31], v[52:53], v[30:31]
	s_waitcnt lgkmcnt(0)
	v_pk_mul_f32 v[16:17], v[30:31], v[16:17]
	v_cvt_f32_f16_sdwa v31, v91 dst_sel:DWORD dst_unused:UNUSED_PAD src0_sel:WORD_1
	v_cvt_f32_f16_e32 v30, v91
	v_cvt_pk_f16_f32 v28, v16, v17
	v_mad_i64_i32 v[16:17], s[0:1], v54, s7, v[32:33]
	v_mul_f32_e32 v52, 0xbfb8aa3b, v30
	v_mul_f32_e32 v53, 0xbfb8aa3b, v31
	v_exp_f32_e32 v52, v52
	v_exp_f32_e32 v53, v53
	s_mov_b64 s[0:1], 0
	v_add_f32_e32 v52, 1.0, v52
	v_add_f32_e32 v53, 1.0, v53
	v_rcp_f32_e32 v52, v52
	v_rcp_f32_e32 v53, v53
	s_nop 0
	v_pk_mul_f32 v[30:31], v[52:53], v[30:31]
	s_nop 0
	v_pk_mul_f32 v[18:19], v[30:31], v[18:19]
	s_nop 0
	v_cvt_pk_f16_f32 v29, v18, v19
	global_store_dwordx4 v[16:17], v[26:29], off sc1
	s_waitcnt lgkmcnt(0)
; __device__ __forceinline__ int crow(int r, int hi) { return (r & 3) + 8 * (r >> 2) + 4 * hi; }
; __device__ __forceinline__ unsigned cvtpk_s(float lo, float hi) { return pg8::cvt_pk_f16(lo, hi); }
; __device__ __forceinline__ int crow(int r, int hi) { return (r & 3) + 8 * (r >> 2) + 4 * hi; }
; template <bool MOBA, int THRL> ...
;     ...
;         for (int d0 = 0; d0 < 2; ++d0) {
; #pragma unroll
;             for (int r = 0; r < 16; ++r) stg[crow(r, le >> 5) * 32 + (le & 31)] = o[d0][r] * rli[r];
;             asm volatile("s_waitcnt lgkmcnt(0)" ::: "memory");
; #pragma unroll
;             for (int i = 0; i < 2; ++i) { const int row = i * 16 + (le >> 2), ch = le & 3;
;                 const f32x4 a0 = *(const f32x4*)(stg + row * 32 + ch * 8), a1 = *(const f32x4*)(stg + row * 32 + ch * 8 + 4);
;                 const h16x8 zv = zpre[d0][i];
;                 float ov[8] = {a0[0], a0[1], a0[2], a0[3], a1[0], a1[1], a1[2], a1[3]};
; #pragma unroll
;                 for (int e = 0; e < 8; ++e) { const float zz = (float)zv[e]; ov[e] *= zz * __builtin_amdgcn_rcpf(1.f + __expf(-zz)); }
;                 u32x4 w; w.x = cvtpk_s(ov[0], ov[1]); w.y = cvtpk_s(ov[2], ov[3]); w.z = cvtpk_s(ov[4], ov[5]); w.w = cvtpk_s(ov[6], ov[7]);
;                 *(u32x4*)(Yw + (long)row * 1536 + d0 * 32 + ch * 8) = w; }
;             asm volatile("s_waitcnt lgkmcnt(0)" ::: "memory");
;         }
;     }
;     asm volatile("s_waitcnt lgkmcnt(0)\n\ts_barrier" ::: "memory");
	ds_write2_b32 v50, v0, v1 offset1:32
	v_mul_f32_e32 v0, v2, v38
	v_mul_f32_e32 v1, v3, v39
	ds_write2_b32 v50, v0, v1 offset0:64 offset1:96
	v_mul_f32_e32 v0, v4, v36
	v_mul_f32_e32 v1, v5, v37
	ds_write2_b32 v51, v0, v1 offset1:32
	v_mul_f32_e32 v0, v6, v34
	v_mul_f32_e32 v1, v7, v35
	ds_write2_b32 v51, v0, v1 offset0:64 offset1:96
	v_mul_f32_e32 v0, v8, v44
	v_mul_f32_e32 v1, v9, v45
	v_cvt_f32_f16_sdwa v9, v84 dst_sel:DWORD dst_unused:UNUSED_PAD src0_sel:WORD_1
	v_cvt_f32_f16_e32 v8, v84
	ds_write2_b32 v22, v0, v1 offset1:32
	v_mul_f32_e32 v0, v10, v42
	v_mul_f32_e32 v1, v11, v43
	v_mul_f32_e32 v10, 0xbfb8aa3b, v8
	v_mul_f32_e32 v11, 0xbfb8aa3b, v9
	v_exp_f32_e32 v10, v10
	v_exp_f32_e32 v11, v11
	ds_write2_b32 v22, v0, v1 offset0:64 offset1:96
	v_mul_f32_e32 v0, v12, v48
	v_mul_f32_e32 v1, v13, v49
	ds_write2_b32 v23, v0, v1 offset1:32
	v_mul_f32_e32 v0, v14, v46
	v_mul_f32_e32 v1, v15, v47
	ds_write2_b32 v23, v0, v1 offset0:64 offset1:96
	v_add_f32_e32 v10, 1.0, v10
	v_add_f32_e32 v11, 1.0, v11
	s_waitcnt lgkmcnt(0)
	v_rcp_f32_e32 v10, v10
	v_rcp_f32_e32 v11, v11
	ds_read_b128 v[4:7], v24 offset:51200
	ds_read_b128 v[0:3], v24 offset:51216
	v_pk_mul_f32 v[8:9], v[10:11], v[8:9]
	s_waitcnt lgkmcnt(1)
	v_pk_mul_f32 v[4:5], v[8:9], v[4:5]
	v_cvt_f32_f16_sdwa v9, v85 dst_sel:DWORD dst_unused:UNUSED_PAD src0_sel:WORD_1
	v_cvt_f32_f16_e32 v8, v85
	v_mul_f32_e32 v11, 0xbfb8aa3b, v9
	v_mul_f32_e32 v10, 0xbfb8aa3b, v8
	v_exp_f32_e32 v10, v10
	v_exp_f32_e32 v11, v11
	v_add_f32_e32 v10, 1.0, v10
	v_add_f32_e32 v11, 1.0, v11
	v_rcp_f32_e32 v10, v10
	v_rcp_f32_e32 v11, v11
	s_nop 0
	v_pk_mul_f32 v[8:9], v[10:11], v[8:9]
	s_nop 0
	v_pk_mul_f32 v[6:7], v[8:9], v[6:7]
	v_cvt_f32_f16_sdwa v9, v86 dst_sel:DWORD dst_unused:UNUSED_PAD src0_sel:WORD_1
	v_cvt_f32_f16_e32 v8, v86
	v_mul_f32_e32 v11, 0xbfb8aa3b, v9
	v_mul_f32_e32 v10, 0xbfb8aa3b, v8
	v_exp_f32_e32 v10, v10
	v_exp_f32_e32 v11, v11
	v_add_f32_e32 v10, 1.0, v10
	v_add_f32_e32 v11, 1.0, v11
	v_rcp_f32_e32 v10, v10
	v_rcp_f32_e32 v11, v11
	s_nop 0
	v_pk_mul_f32 v[8:9], v[10:11], v[8:9]
	s_waitcnt lgkmcnt(0)
	v_pk_mul_f32 v[8:9], v[8:9], v[0:1]
	v_cvt_f32_f16_sdwa v1, v87 dst_sel:DWORD dst_unused:UNUSED_PAD src0_sel:WORD_1
	v_cvt_f32_f16_e32 v0, v87
	v_mul_f32_e32 v11, 0xbfb8aa3b, v1
	v_mul_f32_e32 v10, 0xbfb8aa3b, v0
	v_exp_f32_e32 v10, v10
	v_exp_f32_e32 v11, v11
	v_add_f32_e32 v10, 1.0, v10
	v_add_f32_e32 v11, 1.0, v11
	v_rcp_f32_e32 v10, v10
	v_rcp_f32_e32 v11, v11
	s_nop 0
	v_pk_mul_f32 v[0:1], v[10:11], v[0:1]
	s_nop 0
	v_pk_mul_f32 v[10:11], v[0:1], v[2:3]
	v_cvt_pk_f16_f32 v2, v8, v9
	s_waitcnt vmcnt(2)
	v_cvt_f32_f16_sdwa v9, v80 dst_sel:DWORD dst_unused:UNUSED_PAD src0_sel:WORD_1
	v_cvt_f32_f16_e32 v8, v80
	v_cvt_pk_f16_f32 v3, v10, v11
	v_cvt_pk_f16_f32 v0, v4, v5
	v_mul_f32_e32 v11, 0xbfb8aa3b, v9
	v_mul_f32_e32 v10, 0xbfb8aa3b, v8
	v_exp_f32_e32 v10, v10
	v_exp_f32_e32 v11, v11
	v_cvt_pk_f16_f32 v1, v6, v7
	global_store_dwordx4 v[20:21], v[0:3], off offset:64 sc1
	v_add_f32_e32 v10, 1.0, v10
	v_add_f32_e32 v11, 1.0, v11
	v_rcp_f32_e32 v10, v10
	v_rcp_f32_e32 v11, v11
	ds_read_b128 v[4:7], v25 offset:51200
	ds_read_b128 v[0:3], v25 offset:51216
	v_pk_mul_f32 v[8:9], v[10:11], v[8:9]
	s_waitcnt lgkmcnt(1)
	v_pk_mul_f32 v[4:5], v[8:9], v[4:5]
	v_cvt_f32_f16_sdwa v9, v81 dst_sel:DWORD dst_unused:UNUSED_PAD src0_sel:WORD_1
	v_cvt_f32_f16_e32 v8, v81
	v_mul_f32_e32 v11, 0xbfb8aa3b, v9
	v_mul_f32_e32 v10, 0xbfb8aa3b, v8
	v_exp_f32_e32 v10, v10
	v_exp_f32_e32 v11, v11
	v_add_f32_e32 v10, 1.0, v10
	v_add_f32_e32 v11, 1.0, v11
	v_rcp_f32_e32 v10, v10
	v_rcp_f32_e32 v11, v11
	s_nop 0
	v_pk_mul_f32 v[8:9], v[10:11], v[8:9]
	s_nop 0
	v_pk_mul_f32 v[6:7], v[8:9], v[6:7]
	v_cvt_f32_f16_sdwa v9, v82 dst_sel:DWORD dst_unused:UNUSED_PAD src0_sel:WORD_1
	v_cvt_f32_f16_e32 v8, v82
	v_mul_f32_e32 v11, 0xbfb8aa3b, v9
	v_mul_f32_e32 v10, 0xbfb8aa3b, v8
	v_exp_f32_e32 v10, v10
	v_exp_f32_e32 v11, v11
	v_add_f32_e32 v10, 1.0, v10
	v_add_f32_e32 v11, 1.0, v11
	v_rcp_f32_e32 v10, v10
	v_rcp_f32_e32 v11, v11
	s_nop 0
	v_pk_mul_f32 v[8:9], v[10:11], v[8:9]
	s_waitcnt lgkmcnt(0)
	v_pk_mul_f32 v[8:9], v[8:9], v[0:1]
	v_cvt_f32_f16_sdwa v1, v83 dst_sel:DWORD dst_unused:UNUSED_PAD src0_sel:WORD_1
	v_cvt_f32_f16_e32 v0, v83
	v_mul_f32_e32 v11, 0xbfb8aa3b, v1
	v_mul_f32_e32 v10, 0xbfb8aa3b, v0
	v_exp_f32_e32 v10, v10
	v_exp_f32_e32 v11, v11
	v_add_f32_e32 v10, 1.0, v10
	v_add_f32_e32 v11, 1.0, v11
	v_rcp_f32_e32 v10, v10
	v_rcp_f32_e32 v11, v11
	s_nop 0
	v_pk_mul_f32 v[0:1], v[10:11], v[0:1]
	s_nop 0
	v_pk_mul_f32 v[10:11], v[0:1], v[2:3]
	v_cvt_pk_f16_f32 v0, v4, v5
	v_cvt_pk_f16_f32 v1, v6, v7
	v_cvt_pk_f16_f32 v2, v8, v9
	v_cvt_pk_f16_f32 v3, v10, v11
	global_store_dwordx4 v[16:17], v[0:3], off offset:64 sc1
	s_waitcnt lgkmcnt(0)
	s_waitcnt lgkmcnt(0)
	s_barrier
